# first K-loop iteration peeled for the five hottest GEMM loops: its MFMAs take C=0, so the per-tile accumulator zeroing is gone there
# speedup vs baseline: 1.0084x; 1.0012x over previous
.LBB0_815:
	s_ashr_i32 s45, s44, 31
	s_lshl_b64 s[48:49], s[44:45], 19
	s_add_u32 s48, s8, s48
	s_addc_u32 s49, s10, s49
	s_ashr_i32 s43, s42, 31
	s_lshl_b64 s[50:51], s[42:43], 19
	s_add_u32 s50, s11, s50
	s_addc_u32 s51, s12, s51
	s_andn2_b64 vcc, exec, s[34:35]
	s_cbranch_vccnz .LBB0_823
	v_lshl_add_u32 v156, s52, 8, v149
	v_ashrrev_i32_e32 v157, 31, v156
	v_lshl_add_u64 v[158:159], v[156:157], 2, v[136:137]
	global_load_dword v244, v[158:159], off
	global_load_dword v245, v[158:159], off offset:64
	global_load_dword v246, v[158:159], off offset:128
	global_load_dword v247, v[158:159], off offset:192
	global_load_dword v248, v[158:159], off offset:512
	global_load_dword v249, v[158:159], off offset:576
	global_load_dword v250, v[158:159], off offset:640
	global_load_dword v251, v[158:159], off offset:704
	s_and_b64 s[60:61], s[46:47], exec
	s_cselect_b32 s43, s49, s55
	s_cselect_b32 s45, s48, s54
	s_cselect_b32 s64, s51, s59
	s_cselect_b32 s65, s50, s58
	s_add_u32 s66, s58, 0x100
	s_addc_u32 s68, s59, 0
	s_add_u32 s54, s54, 0x40080
	v_mov_b32_e32 v1, 0x3ecc95a3
	s_addc_u32 s55, s55, 0
	s_mov_b32 s58, 0
.Lpeelph7b_0:
	s_add_i32 s69, s58, 2
	s_add_u32 s59, s54, 0xfffc0080
	s_addc_u32 s60, s55, -1
	s_add_i32 s70, 0, 0x10000
	s_cmp_eq_u32 s53, s58
	s_cselect_b32 s61, s43, s60
	s_cselect_b32 s60, s45, s59
	v_add_u32_e32 v146, s70, v151
	s_cselect_b32 s59, s64, s68
	s_cselect_b32 s58, s65, s66
	s_add_i32 s72, 0, 0x14000
	ds_read_b128 v[142:145], v146
	ds_read_b128 v[156:159], v146 offset:1024
	ds_read_b128 v[160:163], v146 offset:2048
	ds_read_b128 v[170:173], v146 offset:3072
	v_add_u32_e32 v146, s72, v151
	ds_read_b128 v[174:177], v146
	ds_read_b128 v[178:181], v146 offset:1024
	ds_read_b128 v[182:185], v146 offset:2048
	ds_read_b128 v[186:189], v146 offset:3072
	v_lshl_add_u64 v[146:147], s[54:55], 0, v[140:141]
	s_add_i32 m0, s16, 0xc000
	ds_read_b128 v[190:193], v154
	ds_read_b128 v[194:197], v154 offset:1024
	ds_read_b128 v[198:201], v154 offset:2048
	ds_read_b128 v[202:205], v154 offset:3072
	ds_read_b128 v[206:209], v154 offset:4096
	ds_read_b128 v[210:213], v154 offset:5120
	ds_read_b128 v[214:217], v154 offset:6144
	ds_read_b128 v[218:221], v154 offset:7168
	global_load_lds_dwordx4 v[146:147], off
	v_lshl_add_u64 v[146:147], s[54:55], 0, v[138:139]
	s_add_i32 m0, s16, 0xe000
	s_nop 0
	global_load_lds_dwordx4 v[146:147], off
	s_waitcnt vmcnt(8)
	s_waitcnt lgkmcnt(0)
	s_barrier
	s_setprio 1
	s_waitcnt lgkmcnt(0)
	v_mfma_f32_16x16x32_bf16 v[126:129], v[142:145], v[190:193], 0
	v_mfma_f32_16x16x32_bf16 v[118:121], v[160:163], v[190:193], 0
	v_mfma_f32_16x16x32_bf16 v[110:113], v[142:145], v[198:201], 0
	v_mfma_f32_16x16x32_bf16 v[102:105], v[160:163], v[198:201], 0
	v_mfma_f32_16x16x32_bf16 v[94:97], v[142:145], v[206:209], 0
	v_mfma_f32_16x16x32_bf16 v[86:89], v[160:163], v[206:209], 0
	v_mfma_f32_16x16x32_bf16 v[78:81], v[142:145], v[214:217], 0
	v_mfma_f32_16x16x32_bf16 v[70:73], v[160:163], v[214:217], 0
	v_mfma_f32_16x16x32_bf16 v[126:129], v[156:159], v[194:197], v[126:129]
	v_mfma_f32_16x16x32_bf16 v[118:121], v[170:173], v[194:197], v[118:121]
	v_mfma_f32_16x16x32_bf16 v[110:113], v[156:159], v[202:205], v[110:113]
	v_mfma_f32_16x16x32_bf16 v[102:105], v[170:173], v[202:205], v[102:105]
	v_mfma_f32_16x16x32_bf16 v[94:97], v[156:159], v[210:213], v[94:97]
	v_mfma_f32_16x16x32_bf16 v[86:89], v[170:173], v[210:213], v[86:89]
	v_mfma_f32_16x16x32_bf16 v[78:81], v[156:159], v[218:221], v[78:81]
	v_mfma_f32_16x16x32_bf16 v[70:73], v[170:173], v[218:221], v[70:73]
	s_setprio 0
	s_setprio 1
	v_mfma_f32_16x16x32_bf16 v[122:125], v[174:177], v[190:193], 0
	v_mfma_f32_16x16x32_bf16 v[114:117], v[182:185], v[190:193], 0
	v_mfma_f32_16x16x32_bf16 v[106:109], v[174:177], v[198:201], 0
	v_mfma_f32_16x16x32_bf16 v[98:101], v[182:185], v[198:201], 0
	v_mfma_f32_16x16x32_bf16 v[90:93], v[174:177], v[206:209], 0
	v_mfma_f32_16x16x32_bf16 v[82:85], v[182:185], v[206:209], 0
	v_mfma_f32_16x16x32_bf16 v[74:77], v[174:177], v[214:217], 0
	v_mfma_f32_16x16x32_bf16 v[66:69], v[182:185], v[214:217], 0
	v_mfma_f32_16x16x32_bf16 v[122:125], v[178:181], v[194:197], v[122:125]
	v_mfma_f32_16x16x32_bf16 v[114:117], v[186:189], v[194:197], v[114:117]
	v_mfma_f32_16x16x32_bf16 v[106:109], v[178:181], v[202:205], v[106:109]
	v_mfma_f32_16x16x32_bf16 v[98:101], v[186:189], v[202:205], v[98:101]
	v_mfma_f32_16x16x32_bf16 v[90:93], v[178:181], v[210:213], v[90:93]
	v_mfma_f32_16x16x32_bf16 v[82:85], v[186:189], v[210:213], v[82:85]
	v_mfma_f32_16x16x32_bf16 v[74:77], v[178:181], v[218:221], v[74:77]
	v_mfma_f32_16x16x32_bf16 v[66:69], v[186:189], v[218:221], v[66:69]
	s_setprio 0
	s_barrier
	s_add_i32 s70, s70, s14
	v_lshl_add_u64 v[146:147], s[58:59], 0, v[166:167]
	s_mov_b32 m0, s70
	ds_read_b128 v[190:193], v154 offset:16384
	ds_read_b128 v[194:197], v154 offset:17408
	ds_read_b128 v[198:201], v154 offset:18432
	ds_read_b128 v[202:205], v154 offset:19456
	ds_read_b128 v[206:209], v154 offset:20480
	ds_read_b128 v[210:213], v154 offset:21504
	ds_read_b128 v[214:217], v154 offset:22528
	ds_read_b128 v[218:221], v154 offset:23552
	global_load_lds_dwordx4 v[146:147], off
	s_add_i32 m0, s70, 0x2000
	s_add_u32 s70, s58, 0x40000
	v_lshl_add_u64 v[164:165], s[58:59], 0, v[134:135]
	s_addc_u32 s71, s59, 0
	s_add_i32 s72, s72, s14
	global_load_lds_dwordx4 v[164:165], off
	v_lshl_add_u64 v[222:223], s[70:71], 0, v[166:167]
	s_mov_b32 m0, s72
	v_lshl_add_u64 v[232:233], s[60:61], 0, v[130:131]
	global_load_lds_dwordx4 v[222:223], off
	v_lshl_add_u64 v[222:223], s[70:71], 0, v[134:135]
	s_add_i32 m0, s72, 0x2000
	s_nop 0
	global_load_lds_dwordx4 v[222:223], off
	v_lshl_add_u64 v[222:223], s[60:61], 0, v[132:133]
	s_mov_b32 m0, s16
	s_nop 0
	global_load_lds_dwordx4 v[222:223], off
	s_mov_b32 m0, s20
	s_nop 0
	global_load_lds_dwordx4 v[232:233], off
	s_waitcnt vmcnt(8)
	s_waitcnt lgkmcnt(0)
	s_barrier
	s_setprio 1
	s_waitcnt lgkmcnt(0)
	v_mfma_f32_16x16x32_bf16 v[62:65], v[142:145], v[190:193], 0
	v_mfma_f32_16x16x32_bf16 v[54:57], v[160:163], v[190:193], 0
	v_mfma_f32_16x16x32_bf16 v[46:49], v[142:145], v[198:201], 0
	v_mfma_f32_16x16x32_bf16 v[38:41], v[160:163], v[198:201], 0
	v_mfma_f32_16x16x32_bf16 v[30:33], v[142:145], v[206:209], 0
	v_mfma_f32_16x16x32_bf16 v[22:25], v[160:163], v[206:209], 0
	v_mfma_f32_16x16x32_bf16 v[14:17], v[142:145], v[214:217], 0
	v_mfma_f32_16x16x32_bf16 v[6:9], v[160:163], v[214:217], 0
	v_mfma_f32_16x16x32_bf16 v[62:65], v[156:159], v[194:197], v[62:65]
	v_mfma_f32_16x16x32_bf16 v[54:57], v[170:173], v[194:197], v[54:57]
	v_mfma_f32_16x16x32_bf16 v[46:49], v[156:159], v[202:205], v[46:49]
	v_mfma_f32_16x16x32_bf16 v[38:41], v[170:173], v[202:205], v[38:41]
	v_mfma_f32_16x16x32_bf16 v[30:33], v[156:159], v[210:213], v[30:33]
	v_mfma_f32_16x16x32_bf16 v[22:25], v[170:173], v[210:213], v[22:25]
	v_mfma_f32_16x16x32_bf16 v[14:17], v[156:159], v[218:221], v[14:17]
	v_mfma_f32_16x16x32_bf16 v[6:9], v[170:173], v[218:221], v[6:9]
	s_setprio 0
	s_setprio 1
	v_mfma_f32_16x16x32_bf16 v[58:61], v[174:177], v[190:193], 0
	v_mfma_f32_16x16x32_bf16 v[50:53], v[182:185], v[190:193], 0
	v_mfma_f32_16x16x32_bf16 v[42:45], v[174:177], v[198:201], 0
	v_mfma_f32_16x16x32_bf16 v[34:37], v[182:185], v[198:201], 0
	v_mfma_f32_16x16x32_bf16 v[26:29], v[174:177], v[206:209], 0
	v_mfma_f32_16x16x32_bf16 v[18:21], v[182:185], v[206:209], 0
	v_mfma_f32_16x16x32_bf16 v[10:13], v[174:177], v[214:217], 0
	v_mfma_f32_16x16x32_bf16 v[2:5], v[182:185], v[214:217], 0
	v_mfma_f32_16x16x32_bf16 v[58:61], v[178:181], v[194:197], v[58:61]
	v_mfma_f32_16x16x32_bf16 v[50:53], v[186:189], v[194:197], v[50:53]
	v_mfma_f32_16x16x32_bf16 v[42:45], v[178:181], v[202:205], v[42:45]
	v_mfma_f32_16x16x32_bf16 v[34:37], v[186:189], v[202:205], v[34:37]
	v_mfma_f32_16x16x32_bf16 v[26:29], v[178:181], v[210:213], v[26:29]
	v_mfma_f32_16x16x32_bf16 v[18:21], v[186:189], v[210:213], v[18:21]
	v_mfma_f32_16x16x32_bf16 v[10:13], v[178:181], v[218:221], v[10:13]
	v_mfma_f32_16x16x32_bf16 v[2:5], v[186:189], v[218:221], v[2:5]
	s_setprio 0
	s_barrier
	s_add_i32 s70, 0, 0x18000
	v_add_u32_e32 v148, s70, v151
	s_add_i32 s71, 0, 0x1c000
	ds_read_b128 v[142:145], v148
	ds_read_b128 v[156:159], v148 offset:1024
	ds_read_b128 v[160:163], v148 offset:2048
	ds_read_b128 v[170:173], v148 offset:3072
	v_add_u32_e32 v148, s71, v151
	ds_read_b128 v[174:177], v148
	ds_read_b128 v[178:181], v148 offset:1024
	ds_read_b128 v[182:185], v148 offset:2048
	ds_read_b128 v[186:189], v148 offset:3072
	s_add_u32 s60, s60, 0x40000
	s_addc_u32 s61, s61, 0
	s_mov_b32 m0, s21
	v_lshl_add_u64 v[234:235], s[60:61], 0, v[132:133]
	ds_read_b128 v[190:193], v154 offset:32768
	ds_read_b128 v[194:197], v154 offset:33792
	ds_read_b128 v[198:201], v154 offset:34816
	ds_read_b128 v[202:205], v154 offset:35840
	ds_read_b128 v[206:209], v154 offset:36864
	ds_read_b128 v[210:213], v154 offset:37888
	ds_read_b128 v[214:217], v154 offset:38912
	ds_read_b128 v[218:221], v154 offset:39936
	global_load_lds_dwordx4 v[234:235], off
	v_lshl_add_u64 v[234:235], s[60:61], 0, v[130:131]
	s_mov_b32 m0, s22
	s_nop 0
	global_load_lds_dwordx4 v[234:235], off
	s_waitcnt vmcnt(8)
	s_waitcnt lgkmcnt(0)
	s_barrier
	s_setprio 1
	s_waitcnt lgkmcnt(0)
	v_mfma_f32_16x16x32_bf16 v[126:129], v[142:145], v[190:193], v[126:129]
	v_mfma_f32_16x16x32_bf16 v[118:121], v[160:163], v[190:193], v[118:121]
	v_mfma_f32_16x16x32_bf16 v[110:113], v[142:145], v[198:201], v[110:113]
	v_mfma_f32_16x16x32_bf16 v[102:105], v[160:163], v[198:201], v[102:105]
	v_mfma_f32_16x16x32_bf16 v[94:97], v[142:145], v[206:209], v[94:97]
	v_mfma_f32_16x16x32_bf16 v[86:89], v[160:163], v[206:209], v[86:89]
	v_mfma_f32_16x16x32_bf16 v[78:81], v[142:145], v[214:217], v[78:81]
	v_mfma_f32_16x16x32_bf16 v[70:73], v[160:163], v[214:217], v[70:73]
	v_mfma_f32_16x16x32_bf16 v[126:129], v[156:159], v[194:197], v[126:129]
	v_mfma_f32_16x16x32_bf16 v[118:121], v[170:173], v[194:197], v[118:121]
	v_mfma_f32_16x16x32_bf16 v[110:113], v[156:159], v[202:205], v[110:113]
	v_mfma_f32_16x16x32_bf16 v[102:105], v[170:173], v[202:205], v[102:105]
	v_mfma_f32_16x16x32_bf16 v[94:97], v[156:159], v[210:213], v[94:97]
	v_mfma_f32_16x16x32_bf16 v[86:89], v[170:173], v[210:213], v[86:89]
	v_mfma_f32_16x16x32_bf16 v[78:81], v[156:159], v[218:221], v[78:81]
	v_mfma_f32_16x16x32_bf16 v[70:73], v[170:173], v[218:221], v[70:73]
	s_setprio 0
	s_setprio 1
	v_mfma_f32_16x16x32_bf16 v[122:125], v[174:177], v[190:193], v[122:125]
	v_mfma_f32_16x16x32_bf16 v[114:117], v[182:185], v[190:193], v[114:117]
	v_mfma_f32_16x16x32_bf16 v[106:109], v[174:177], v[198:201], v[106:109]
	v_mfma_f32_16x16x32_bf16 v[98:101], v[182:185], v[198:201], v[98:101]
	v_mfma_f32_16x16x32_bf16 v[90:93], v[174:177], v[206:209], v[90:93]
	v_mfma_f32_16x16x32_bf16 v[82:85], v[182:185], v[206:209], v[82:85]
	v_mfma_f32_16x16x32_bf16 v[74:77], v[174:177], v[214:217], v[74:77]
	v_mfma_f32_16x16x32_bf16 v[66:69], v[182:185], v[214:217], v[66:69]
	v_mfma_f32_16x16x32_bf16 v[122:125], v[178:181], v[194:197], v[122:125]
	v_mfma_f32_16x16x32_bf16 v[114:117], v[186:189], v[194:197], v[114:117]
	v_mfma_f32_16x16x32_bf16 v[106:109], v[178:181], v[202:205], v[106:109]
	v_mfma_f32_16x16x32_bf16 v[98:101], v[186:189], v[202:205], v[98:101]
	v_mfma_f32_16x16x32_bf16 v[90:93], v[178:181], v[210:213], v[90:93]
	v_mfma_f32_16x16x32_bf16 v[82:85], v[186:189], v[210:213], v[82:85]
	v_mfma_f32_16x16x32_bf16 v[74:77], v[178:181], v[218:221], v[74:77]
	v_mfma_f32_16x16x32_bf16 v[66:69], v[186:189], v[218:221], v[66:69]
	s_setprio 0
	s_barrier
	s_add_i32 s60, s70, s14
	v_lshl_add_u64 v[146:147], v[146:147], 0, s[56:57]
	s_mov_b32 m0, s60
	ds_read_b128 v[190:193], v154 offset:49152
	ds_read_b128 v[194:197], v154 offset:50176
	ds_read_b128 v[198:201], v154 offset:51200
	ds_read_b128 v[202:205], v154 offset:52224
	ds_read_b128 v[206:209], v154 offset:53248
	ds_read_b128 v[210:213], v154 offset:54272
	ds_read_b128 v[214:217], v154 offset:55296
	ds_read_b128 v[218:221], v154 offset:56320
	global_load_lds_dwordx4 v[146:147], off
	s_add_i32 m0, s60, 0x2000
	s_add_u32 s58, s58, 0x40080
	v_lshl_add_u64 v[146:147], v[164:165], 0, s[56:57]
	s_addc_u32 s59, s59, 0
	s_add_i32 s60, s71, s14
	global_load_lds_dwordx4 v[146:147], off
	v_lshl_add_u64 v[146:147], s[58:59], 0, v[166:167]
	s_mov_b32 m0, s60
	s_nop 0
	global_load_lds_dwordx4 v[146:147], off
	v_lshl_add_u64 v[146:147], s[58:59], 0, v[134:135]
	s_add_i32 m0, s60, 0x2000
	s_nop 0
	global_load_lds_dwordx4 v[146:147], off
	v_lshl_add_u64 v[146:147], v[222:223], 0, s[56:57]
	s_mov_b32 m0, s23
	s_nop 0
	global_load_lds_dwordx4 v[146:147], off
	v_lshl_add_u64 v[146:147], v[232:233], 0, s[56:57]
	s_mov_b32 m0, s24
	s_nop 0
	global_load_lds_dwordx4 v[146:147], off
	s_waitcnt vmcnt(8)
	s_waitcnt lgkmcnt(0)
	s_barrier
	s_setprio 1
	s_waitcnt lgkmcnt(0)
	v_mfma_f32_16x16x32_bf16 v[62:65], v[142:145], v[190:193], v[62:65]
	v_mfma_f32_16x16x32_bf16 v[54:57], v[160:163], v[190:193], v[54:57]
	v_mfma_f32_16x16x32_bf16 v[46:49], v[142:145], v[198:201], v[46:49]
	v_mfma_f32_16x16x32_bf16 v[38:41], v[160:163], v[198:201], v[38:41]
	v_mfma_f32_16x16x32_bf16 v[30:33], v[142:145], v[206:209], v[30:33]
	v_mfma_f32_16x16x32_bf16 v[22:25], v[160:163], v[206:209], v[22:25]
	v_mfma_f32_16x16x32_bf16 v[14:17], v[142:145], v[214:217], v[14:17]
	v_mfma_f32_16x16x32_bf16 v[6:9], v[160:163], v[214:217], v[6:9]
	v_mfma_f32_16x16x32_bf16 v[62:65], v[156:159], v[194:197], v[62:65]
	v_mfma_f32_16x16x32_bf16 v[54:57], v[170:173], v[194:197], v[54:57]
	v_mfma_f32_16x16x32_bf16 v[46:49], v[156:159], v[202:205], v[46:49]
	v_mfma_f32_16x16x32_bf16 v[38:41], v[170:173], v[202:205], v[38:41]
	v_mfma_f32_16x16x32_bf16 v[30:33], v[156:159], v[210:213], v[30:33]
	v_mfma_f32_16x16x32_bf16 v[22:25], v[170:173], v[210:213], v[22:25]
	v_mfma_f32_16x16x32_bf16 v[14:17], v[156:159], v[218:221], v[14:17]
	v_mfma_f32_16x16x32_bf16 v[6:9], v[170:173], v[218:221], v[6:9]
	s_setprio 0
	s_setprio 1
	v_mfma_f32_16x16x32_bf16 v[58:61], v[174:177], v[190:193], v[58:61]
	v_mfma_f32_16x16x32_bf16 v[50:53], v[182:185], v[190:193], v[50:53]
	v_mfma_f32_16x16x32_bf16 v[42:45], v[174:177], v[198:201], v[42:45]
	v_mfma_f32_16x16x32_bf16 v[34:37], v[182:185], v[198:201], v[34:37]
	v_mfma_f32_16x16x32_bf16 v[26:29], v[174:177], v[206:209], v[26:29]
	v_mfma_f32_16x16x32_bf16 v[18:21], v[182:185], v[206:209], v[18:21]
	v_mfma_f32_16x16x32_bf16 v[10:13], v[174:177], v[214:217], v[10:13]
	v_mfma_f32_16x16x32_bf16 v[2:5], v[182:185], v[214:217], v[2:5]
	v_mfma_f32_16x16x32_bf16 v[58:61], v[178:181], v[194:197], v[58:61]
	v_mfma_f32_16x16x32_bf16 v[50:53], v[186:189], v[194:197], v[50:53]
	v_mfma_f32_16x16x32_bf16 v[42:45], v[178:181], v[202:205], v[42:45]
	v_mfma_f32_16x16x32_bf16 v[34:37], v[186:189], v[202:205], v[34:37]
	v_mfma_f32_16x16x32_bf16 v[26:29], v[178:181], v[210:213], v[26:29]
	v_mfma_f32_16x16x32_bf16 v[18:21], v[186:189], v[210:213], v[18:21]
	v_mfma_f32_16x16x32_bf16 v[10:13], v[178:181], v[218:221], v[10:13]
	v_mfma_f32_16x16x32_bf16 v[2:5], v[186:189], v[218:221], v[2:5]
	s_setprio 0
	s_barrier
	s_add_u32 s66, s66, 0x100
	s_addc_u32 s68, s68, 0
	s_add_u32 s54, s54, 0x100
	s_addc_u32 s55, s55, 0
	s_cmp_ge_i32 s69, s13
	s_mov_b32 s58, s69
	s_cbranch_scc0 .LBB0_817
	s_branch .Lpeelexitph7b

.Lpeelexitph7b:
	s_mov_b64 s[72:73], 0xe800000
	s_mov_b64 s[70:71], 0xe800800
	v_mov_b32_e32 v209, v1
	s_and_b64 vcc, exec, s[36:37]
	s_cbranch_vccz .LBB0_820

.Lpeelph7f_0:
	s_add_i32 s66, s54, 2
	s_add_u32 s55, s52, 0xfffe0080
	s_addc_u32 s58, s53, -1
	s_add_i32 s68, 0, 0x10000
	s_cmp_eq_u32 s51, s54
	s_cselect_b32 s59, s41, s58
	s_cselect_b32 s58, s43, s55
	s_cselect_b32 s55, s62, s65
	s_cselect_b32 s54, s63, s64
	s_add_i32 s69, 0, 0x14000
	v_add_u32_e32 v2, s68, v196
	v_add_u32_e32 v6, s69, v196
	ds_read_b128 v[26:29], v2
	ds_read_b128 v[30:33], v2 offset:1024
	ds_read_b128 v[18:21], v2 offset:2048
	ds_read_b128 v[22:25], v2 offset:3072
	ds_read_b128 v[10:13], v6
	ds_read_b128 v[14:17], v6 offset:1024
	ds_read_b128 v[2:5], v6 offset:2048
	ds_read_b128 v[6:9], v6 offset:3072
	v_lshl_add_u64 v[170:171], s[52:53], 0, v[184:185]
	s_add_i32 m0, s16, 0xc000
	ds_read_b128 v[186:189], v198
	ds_read_b128 v[190:193], v198 offset:1024
	ds_read_b128 v[200:203], v198 offset:2048
	ds_read_b128 v[204:207], v198 offset:3072
	ds_read_b128 v[208:211], v198 offset:4096
	ds_read_b128 v[212:215], v198 offset:5120
	ds_read_b128 v[216:219], v198 offset:6144
	ds_read_b128 v[220:223], v198 offset:7168
	global_load_lds_dwordx4 v[170:171], off
	v_lshl_add_u64 v[170:171], s[52:53], 0, v[182:183]
	s_add_i32 m0, s16, 0xe000
	s_nop 0
	global_load_lds_dwordx4 v[170:171], off
	s_waitcnt vmcnt(8)
	s_waitcnt lgkmcnt(0)
	s_barrier
	s_setprio 1
	s_waitcnt lgkmcnt(0)
	v_mfma_scale_f32_16x16x128_f8f6f4 v[158:161], v[26:33], v[186:193], 0, v194, v169 op_sel_hi:[0,0,0]
	v_mfma_scale_f32_16x16x128_f8f6f4 v[150:153], v[18:25], v[186:193], 0, v194, v169 op_sel_hi:[0,0,0]
	v_mfma_scale_f32_16x16x128_f8f6f4 v[142:145], v[26:33], v[200:207], 0, v194, v169 op_sel_hi:[0,0,0]
	v_mfma_scale_f32_16x16x128_f8f6f4 v[134:137], v[18:25], v[200:207], 0, v194, v169 op_sel_hi:[0,0,0]
	v_mfma_scale_f32_16x16x128_f8f6f4 v[126:129], v[26:33], v[208:215], 0, v194, v169 op_sel_hi:[0,0,0]
	v_mfma_scale_f32_16x16x128_f8f6f4 v[118:121], v[18:25], v[208:215], 0, v194, v169 op_sel_hi:[0,0,0]
	v_mfma_scale_f32_16x16x128_f8f6f4 v[110:113], v[26:33], v[216:223], 0, v194, v169 op_sel_hi:[0,0,0]
	v_mfma_scale_f32_16x16x128_f8f6f4 v[102:105], v[18:25], v[216:223], 0, v194, v169 op_sel_hi:[0,0,0]
	s_setprio 0
	s_setprio 1
	v_mfma_scale_f32_16x16x128_f8f6f4 v[154:157], v[10:17], v[186:193], 0, v194, v169 op_sel_hi:[0,0,0]
	v_mfma_scale_f32_16x16x128_f8f6f4 v[146:149], v[2:9], v[186:193], 0, v194, v169 op_sel_hi:[0,0,0]
	v_mfma_scale_f32_16x16x128_f8f6f4 v[138:141], v[10:17], v[200:207], 0, v194, v169 op_sel_hi:[0,0,0]
	v_mfma_scale_f32_16x16x128_f8f6f4 v[130:133], v[2:9], v[200:207], 0, v194, v169 op_sel_hi:[0,0,0]
	v_mfma_scale_f32_16x16x128_f8f6f4 v[122:125], v[10:17], v[208:215], 0, v194, v169 op_sel_hi:[0,0,0]
	v_mfma_scale_f32_16x16x128_f8f6f4 v[114:117], v[2:9], v[208:215], 0, v194, v169 op_sel_hi:[0,0,0]
	v_mfma_scale_f32_16x16x128_f8f6f4 v[106:109], v[10:17], v[216:223], 0, v194, v169 op_sel_hi:[0,0,0]
	v_mfma_scale_f32_16x16x128_f8f6f4 v[98:101], v[2:9], v[216:223], 0, v194, v169 op_sel_hi:[0,0,0]
	s_setprio 0
	s_barrier
	s_add_i32 s68, s68, s14
	v_lshl_add_u64 v[186:187], s[54:55], 0, v[166:167]
	s_mov_b32 m0, s68
	ds_read_b128 v[200:203], v198 offset:16384
	ds_read_b128 v[204:207], v198 offset:17408
	ds_read_b128 v[208:211], v198 offset:18432
	ds_read_b128 v[212:215], v198 offset:19456
	ds_read_b128 v[216:219], v198 offset:20480
	ds_read_b128 v[220:223], v198 offset:21504
	ds_read_b128 v[236:239], v198 offset:22528
	ds_read_b128 v[240:243], v198 offset:23552
	global_load_lds_dwordx4 v[186:187], off
	s_add_i32 m0, s68, 0x2000
	s_add_u32 s70, s54, 0x20000
	v_lshl_add_u64 v[188:189], s[54:55], 0, v[178:179]
	s_addc_u32 s71, s55, 0
	s_add_i32 s68, s69, s14
	global_load_lds_dwordx4 v[188:189], off
	v_lshl_add_u64 v[170:171], s[70:71], 0, v[166:167]
	s_mov_b32 m0, s68
	v_lshl_add_u64 v[190:191], s[58:59], 0, v[164:165]
	global_load_lds_dwordx4 v[170:171], off
	v_lshl_add_u64 v[170:171], s[70:71], 0, v[178:179]
	s_add_i32 m0, s68, 0x2000
	v_lshl_add_u64 v[192:193], s[58:59], 0, v[162:163]
	global_load_lds_dwordx4 v[170:171], off
	s_mov_b32 m0, s16
	s_nop 0
	global_load_lds_dwordx4 v[190:191], off
	s_mov_b32 m0, s20
	s_nop 0
	global_load_lds_dwordx4 v[192:193], off
	s_waitcnt vmcnt(8)
	s_waitcnt lgkmcnt(0)
	s_barrier
	s_setprio 1
	s_waitcnt lgkmcnt(0)
	v_mfma_scale_f32_16x16x128_f8f6f4 v[94:97], v[26:33], v[200:207], 0, v194, v169 op_sel_hi:[0,0,0]
	v_mfma_scale_f32_16x16x128_f8f6f4 v[86:89], v[18:25], v[200:207], 0, v194, v169 op_sel_hi:[0,0,0]
	v_mfma_scale_f32_16x16x128_f8f6f4 v[78:81], v[26:33], v[208:215], 0, v194, v169 op_sel_hi:[0,0,0]
	v_mfma_scale_f32_16x16x128_f8f6f4 v[70:73], v[18:25], v[208:215], 0, v194, v169 op_sel_hi:[0,0,0]
	v_mfma_scale_f32_16x16x128_f8f6f4 v[62:65], v[26:33], v[216:223], 0, v194, v169 op_sel_hi:[0,0,0]
	v_mfma_scale_f32_16x16x128_f8f6f4 v[54:57], v[18:25], v[216:223], 0, v194, v169 op_sel_hi:[0,0,0]
	v_mfma_scale_f32_16x16x128_f8f6f4 v[46:49], v[26:33], v[236:243], 0, v194, v169 op_sel_hi:[0,0,0]
	v_mfma_scale_f32_16x16x128_f8f6f4 v[38:41], v[18:25], v[236:243], 0, v194, v169 op_sel_hi:[0,0,0]
	s_setprio 0
	s_setprio 1
	v_mfma_scale_f32_16x16x128_f8f6f4 v[90:93], v[10:17], v[200:207], 0, v194, v169 op_sel_hi:[0,0,0]
	v_mfma_scale_f32_16x16x128_f8f6f4 v[82:85], v[2:9], v[200:207], 0, v194, v169 op_sel_hi:[0,0,0]
	v_mfma_scale_f32_16x16x128_f8f6f4 v[74:77], v[10:17], v[208:215], 0, v194, v169 op_sel_hi:[0,0,0]
	v_mfma_scale_f32_16x16x128_f8f6f4 v[66:69], v[2:9], v[208:215], 0, v194, v169 op_sel_hi:[0,0,0]
	v_mfma_scale_f32_16x16x128_f8f6f4 v[58:61], v[10:17], v[216:223], 0, v194, v169 op_sel_hi:[0,0,0]
	v_mfma_scale_f32_16x16x128_f8f6f4 v[50:53], v[2:9], v[216:223], 0, v194, v169 op_sel_hi:[0,0,0]
	v_mfma_scale_f32_16x16x128_f8f6f4 v[42:45], v[10:17], v[236:243], 0, v194, v169 op_sel_hi:[0,0,0]
	v_mfma_scale_f32_16x16x128_f8f6f4 v[34:37], v[2:9], v[236:243], 0, v194, v169 op_sel_hi:[0,0,0]
	s_setprio 0
	s_barrier
	s_add_i32 s68, 0, 0x18000
	s_add_i32 s69, 0, 0x1c000
	v_add_u32_e32 v2, s68, v196
	v_add_u32_e32 v6, s69, v196
	ds_read_b128 v[26:29], v2
	ds_read_b128 v[30:33], v2 offset:1024
	ds_read_b128 v[18:21], v2 offset:2048
	ds_read_b128 v[22:25], v2 offset:3072
	ds_read_b128 v[10:13], v6
	ds_read_b128 v[14:17], v6 offset:1024
	ds_read_b128 v[2:5], v6 offset:2048
	ds_read_b128 v[6:9], v6 offset:3072
	s_add_u32 s58, s58, 0x20000
	s_addc_u32 s59, s59, 0
	s_mov_b32 m0, s21
	v_lshl_add_u64 v[170:171], s[58:59], 0, v[164:165]
	ds_read_b128 v[200:203], v198 offset:32768
	ds_read_b128 v[204:207], v198 offset:33792
	ds_read_b128 v[208:211], v198 offset:34816
	ds_read_b128 v[212:215], v198 offset:35840
	ds_read_b128 v[216:219], v198 offset:36864
	ds_read_b128 v[220:223], v198 offset:37888
	ds_read_b128 v[236:239], v198 offset:38912
	ds_read_b128 v[240:243], v198 offset:39936
	global_load_lds_dwordx4 v[170:171], off
	v_lshl_add_u64 v[170:171], s[58:59], 0, v[162:163]
	s_mov_b32 m0, s22
	s_nop 0
	global_load_lds_dwordx4 v[170:171], off
	s_waitcnt vmcnt(8)
	s_waitcnt lgkmcnt(0)
	s_barrier
	s_setprio 1
	s_waitcnt lgkmcnt(0)
	v_mfma_scale_f32_16x16x128_f8f6f4 v[158:161], v[26:33], v[200:207], v[158:161], v194, v169 op_sel_hi:[0,0,0]
	v_mfma_scale_f32_16x16x128_f8f6f4 v[150:153], v[18:25], v[200:207], v[150:153], v194, v169 op_sel_hi:[0,0,0]
	v_mfma_scale_f32_16x16x128_f8f6f4 v[142:145], v[26:33], v[208:215], v[142:145], v194, v169 op_sel_hi:[0,0,0]
	v_mfma_scale_f32_16x16x128_f8f6f4 v[134:137], v[18:25], v[208:215], v[134:137], v194, v169 op_sel_hi:[0,0,0]
	v_mfma_scale_f32_16x16x128_f8f6f4 v[126:129], v[26:33], v[216:223], v[126:129], v194, v169 op_sel_hi:[0,0,0]
	v_mfma_scale_f32_16x16x128_f8f6f4 v[118:121], v[18:25], v[216:223], v[118:121], v194, v169 op_sel_hi:[0,0,0]
	v_mfma_scale_f32_16x16x128_f8f6f4 v[110:113], v[26:33], v[236:243], v[110:113], v194, v169 op_sel_hi:[0,0,0]
	v_mfma_scale_f32_16x16x128_f8f6f4 v[102:105], v[18:25], v[236:243], v[102:105], v194, v169 op_sel_hi:[0,0,0]
	s_setprio 0
	s_setprio 1
	v_mfma_scale_f32_16x16x128_f8f6f4 v[154:157], v[10:17], v[200:207], v[154:157], v194, v169 op_sel_hi:[0,0,0]
	v_mfma_scale_f32_16x16x128_f8f6f4 v[146:149], v[2:9], v[200:207], v[146:149], v194, v169 op_sel_hi:[0,0,0]
	v_mfma_scale_f32_16x16x128_f8f6f4 v[138:141], v[10:17], v[208:215], v[138:141], v194, v169 op_sel_hi:[0,0,0]
	v_mfma_scale_f32_16x16x128_f8f6f4 v[130:133], v[2:9], v[208:215], v[130:133], v194, v169 op_sel_hi:[0,0,0]
	v_mfma_scale_f32_16x16x128_f8f6f4 v[122:125], v[10:17], v[216:223], v[122:125], v194, v169 op_sel_hi:[0,0,0]
	v_mfma_scale_f32_16x16x128_f8f6f4 v[114:117], v[2:9], v[216:223], v[114:117], v194, v169 op_sel_hi:[0,0,0]
	v_mfma_scale_f32_16x16x128_f8f6f4 v[106:109], v[10:17], v[236:243], v[106:109], v194, v169 op_sel_hi:[0,0,0]
	v_mfma_scale_f32_16x16x128_f8f6f4 v[98:101], v[2:9], v[236:243], v[98:101], v194, v169 op_sel_hi:[0,0,0]
	s_setprio 0
	s_barrier
	s_add_i32 s58, s68, s14
	v_lshl_add_u64 v[170:171], v[186:187], 0, s[56:57]
	s_mov_b32 m0, s58
	ds_read_b128 v[200:203], v198 offset:49152
	ds_read_b128 v[204:207], v198 offset:50176
	ds_read_b128 v[208:211], v198 offset:51200
	ds_read_b128 v[212:215], v198 offset:52224
	ds_read_b128 v[216:219], v198 offset:53248
	ds_read_b128 v[220:223], v198 offset:54272
	ds_read_b128 v[236:239], v198 offset:55296
	ds_read_b128 v[240:243], v198 offset:56320
	global_load_lds_dwordx4 v[170:171], off
	s_add_i32 m0, s58, 0x2000
	s_add_u32 s54, s54, 0x20080
	v_lshl_add_u64 v[170:171], v[188:189], 0, s[56:57]
	s_addc_u32 s55, s55, 0
	s_add_i32 s58, s69, s14
	global_load_lds_dwordx4 v[170:171], off
	v_lshl_add_u64 v[170:171], s[54:55], 0, v[166:167]
	s_mov_b32 m0, s58
	s_nop 0
	global_load_lds_dwordx4 v[170:171], off
	v_lshl_add_u64 v[170:171], s[54:55], 0, v[178:179]
	s_add_i32 m0, s58, 0x2000
	s_nop 0
	global_load_lds_dwordx4 v[170:171], off
	v_lshl_add_u64 v[170:171], v[190:191], 0, s[56:57]
	s_mov_b32 m0, s23
	s_nop 0
	global_load_lds_dwordx4 v[170:171], off
	v_lshl_add_u64 v[170:171], v[192:193], 0, s[56:57]
	s_mov_b32 m0, s24
	s_nop 0
	global_load_lds_dwordx4 v[170:171], off
	s_waitcnt vmcnt(8)
	s_waitcnt lgkmcnt(0)
	s_barrier
	s_setprio 1
	s_waitcnt lgkmcnt(0)
	v_mfma_scale_f32_16x16x128_f8f6f4 v[94:97], v[26:33], v[200:207], v[94:97], v194, v169 op_sel_hi:[0,0,0]
	v_mfma_scale_f32_16x16x128_f8f6f4 v[86:89], v[18:25], v[200:207], v[86:89], v194, v169 op_sel_hi:[0,0,0]
	v_mfma_scale_f32_16x16x128_f8f6f4 v[78:81], v[26:33], v[208:215], v[78:81], v194, v169 op_sel_hi:[0,0,0]
	v_mfma_scale_f32_16x16x128_f8f6f4 v[70:73], v[18:25], v[208:215], v[70:73], v194, v169 op_sel_hi:[0,0,0]
	v_mfma_scale_f32_16x16x128_f8f6f4 v[62:65], v[26:33], v[216:223], v[62:65], v194, v169 op_sel_hi:[0,0,0]
	v_mfma_scale_f32_16x16x128_f8f6f4 v[54:57], v[18:25], v[216:223], v[54:57], v194, v169 op_sel_hi:[0,0,0]
	v_mfma_scale_f32_16x16x128_f8f6f4 v[46:49], v[26:33], v[236:243], v[46:49], v194, v169 op_sel_hi:[0,0,0]
	v_mfma_scale_f32_16x16x128_f8f6f4 v[38:41], v[18:25], v[236:243], v[38:41], v194, v169 op_sel_hi:[0,0,0]
	s_setprio 0
	s_setprio 1
	v_mfma_scale_f32_16x16x128_f8f6f4 v[90:93], v[10:17], v[200:207], v[90:93], v194, v169 op_sel_hi:[0,0,0]
	v_mfma_scale_f32_16x16x128_f8f6f4 v[82:85], v[2:9], v[200:207], v[82:85], v194, v169 op_sel_hi:[0,0,0]
	v_mfma_scale_f32_16x16x128_f8f6f4 v[74:77], v[10:17], v[208:215], v[74:77], v194, v169 op_sel_hi:[0,0,0]
	v_mfma_scale_f32_16x16x128_f8f6f4 v[66:69], v[2:9], v[208:215], v[66:69], v194, v169 op_sel_hi:[0,0,0]
	v_mfma_scale_f32_16x16x128_f8f6f4 v[58:61], v[10:17], v[216:223], v[58:61], v194, v169 op_sel_hi:[0,0,0]
	v_mfma_scale_f32_16x16x128_f8f6f4 v[50:53], v[2:9], v[216:223], v[50:53], v194, v169 op_sel_hi:[0,0,0]
	v_mfma_scale_f32_16x16x128_f8f6f4 v[42:45], v[10:17], v[236:243], v[42:45], v194, v169 op_sel_hi:[0,0,0]
	v_mfma_scale_f32_16x16x128_f8f6f4 v[34:37], v[2:9], v[236:243], v[34:37], v194, v169 op_sel_hi:[0,0,0]
	s_setprio 0
	s_barrier
	s_add_u32 s64, s64, 0x100
	s_addc_u32 s65, s65, 0
	s_add_u32 s52, s52, 0x100
	s_addc_u32 s53, s53, 0
	s_cmp_ge_i32 s66, s13
	s_mov_b32 s54, s66
	s_cbranch_scc0 .LBB0_842
	s_branch .Lpeelexitph7f

.Lpeelexitph7f:
	s_mov_b64 s[70:71], 0xe800800
	v_mov_b32_e32 v209, v1
	s_and_b64 vcc, exec, s[36:37]
	s_cbranch_vccz .LBB0_845

.LBB0_1014:
	s_ashr_i32 s27, s26, 31
	s_lshl_b64 s[0:1], s[26:27], 18
	s_add_u32 s30, s90, s0
	s_addc_u32 s31, s91, s1
	s_ashr_i32 s65, s64, 31
	s_lshl_b64 s[0:1], s[64:65], 18
	s_add_u32 s34, s76, s0
	s_addc_u32 s35, s77, s1
	s_andn2_b64 vcc, exec, s[50:51]
	s_cbranch_vccnz .LBB0_1078
	v_lshl_add_u32 v2, s36, 8, v220
	v_ashrrev_i32_e32 v3, 31, v2
	v_lshl_add_u64 v[4:5], v[2:3], 2, v[186:187]
	global_load_dword v172, v[4:5], off
	global_load_dword v173, v[4:5], off offset:64
	global_load_dword v174, v[4:5], off offset:128
	global_load_dword v175, v[4:5], off offset:192
	global_load_dword v176, v[4:5], off offset:512
	global_load_dword v177, v[4:5], off offset:576
	global_load_dword v223, v[4:5], off offset:640
	global_load_dword v232, v[4:5], off offset:704
	s_and_b64 s[0:1], s[28:29], exec
	s_cselect_b32 s0, s31, s39
	s_cselect_b32 s1, s30, s38
	s_cselect_b32 s8, s35, s41
	s_cselect_b32 s11, s34, s40
	s_add_u32 s16, s40, 0x100
	s_addc_u32 s19, s41, 0
	s_add_u32 s38, s38, 0x20080
	v_mov_b32_e32 v1, 0x3ecc95a3
	s_addc_u32 s39, s39, 0
	s_mov_b32 s37, 0
.Lpeelph9_0:
	s_add_i32 s27, s37, 2
	s_add_u32 s40, s38, 0xfffe0080
	s_addc_u32 s41, s39, -1
	s_add_i32 s65, 0, 0x10000
	s_cmp_eq_u32 s95, s37
	s_cselect_b32 s69, s0, s41
	s_cselect_b32 s68, s1, s40
	s_cselect_b32 s41, s8, s19
	s_cselect_b32 s40, s11, s16
	s_add_i32 s37, 0, 0x14000
	v_add_u32_e32 v2, s65, v221
	v_add_u32_e32 v6, s37, v221
	ds_read_b128 v[26:29], v2
	ds_read_b128 v[30:33], v2 offset:1024
	ds_read_b128 v[18:21], v2 offset:2048
	ds_read_b128 v[22:25], v2 offset:3072
	ds_read_b128 v[10:13], v6
	ds_read_b128 v[14:17], v6 offset:1024
	ds_read_b128 v[2:5], v6 offset:2048
	ds_read_b128 v[6:9], v6 offset:3072
	v_lshl_add_u64 v[170:171], s[38:39], 0, v[192:193]
	s_add_i32 m0, s21, 0xc000
	ds_read_b128 v[194:197], v222
	ds_read_b128 v[198:201], v222 offset:1024
	ds_read_b128 v[202:205], v222 offset:2048
	ds_read_b128 v[206:209], v222 offset:3072
	ds_read_b128 v[210:213], v222 offset:4096
	ds_read_b128 v[214:217], v222 offset:5120
	ds_read_b128 v[236:239], v222 offset:6144
	ds_read_b128 v[240:243], v222 offset:7168
	global_load_lds_dwordx4 v[170:171], off
	v_lshl_add_u64 v[170:171], s[38:39], 0, v[190:191]
	s_add_i32 m0, s21, 0xe000
	s_nop 0
	global_load_lds_dwordx4 v[170:171], off
	s_waitcnt vmcnt(8)
	s_waitcnt lgkmcnt(0)
	s_barrier
	s_setprio 1
	s_waitcnt lgkmcnt(0)
	v_mfma_scale_f32_16x16x128_f8f6f4 v[94:97], v[26:33], v[194:201], 0, v183, v169 op_sel_hi:[0,0,0]
	v_mfma_scale_f32_16x16x128_f8f6f4 v[90:93], v[18:25], v[194:201], 0, v183, v169 op_sel_hi:[0,0,0]
	v_mfma_scale_f32_16x16x128_f8f6f4 v[86:89], v[26:33], v[202:209], 0, v183, v169 op_sel_hi:[0,0,0]
	v_mfma_scale_f32_16x16x128_f8f6f4 v[82:85], v[18:25], v[202:209], 0, v183, v169 op_sel_hi:[0,0,0]
	v_mfma_scale_f32_16x16x128_f8f6f4 v[78:81], v[26:33], v[210:217], 0, v183, v169 op_sel_hi:[0,0,0]
	v_mfma_scale_f32_16x16x128_f8f6f4 v[74:77], v[18:25], v[210:217], 0, v183, v169 op_sel_hi:[0,0,0]
	v_mfma_scale_f32_16x16x128_f8f6f4 v[70:73], v[26:33], v[236:243], 0, v183, v169 op_sel_hi:[0,0,0]
	v_mfma_scale_f32_16x16x128_f8f6f4 v[66:69], v[18:25], v[236:243], 0, v183, v169 op_sel_hi:[0,0,0]
	s_setprio 0
	s_setprio 1
	v_mfma_scale_f32_16x16x128_f8f6f4 v[158:161], v[10:17], v[194:201], 0, v183, v169 op_sel_hi:[0,0,0]
	v_mfma_scale_f32_16x16x128_f8f6f4 v[154:157], v[2:9], v[194:201], 0, v183, v169 op_sel_hi:[0,0,0]
	v_mfma_scale_f32_16x16x128_f8f6f4 v[150:153], v[10:17], v[202:209], 0, v183, v169 op_sel_hi:[0,0,0]
	v_mfma_scale_f32_16x16x128_f8f6f4 v[146:149], v[2:9], v[202:209], 0, v183, v169 op_sel_hi:[0,0,0]
	v_mfma_scale_f32_16x16x128_f8f6f4 v[142:145], v[10:17], v[210:217], 0, v183, v169 op_sel_hi:[0,0,0]
	v_mfma_scale_f32_16x16x128_f8f6f4 v[138:141], v[2:9], v[210:217], 0, v183, v169 op_sel_hi:[0,0,0]
	v_mfma_scale_f32_16x16x128_f8f6f4 v[134:137], v[10:17], v[236:243], 0, v183, v169 op_sel_hi:[0,0,0]
	v_mfma_scale_f32_16x16x128_f8f6f4 v[130:133], v[2:9], v[236:243], 0, v183, v169 op_sel_hi:[0,0,0]
	s_setprio 0
	s_barrier
	s_add_i32 s65, s65, s20
	v_lshl_add_u64 v[194:195], s[40:41], 0, v[162:163]
	s_mov_b32 m0, s65
	ds_read_b128 v[202:205], v222 offset:16384
	ds_read_b128 v[206:209], v222 offset:17408
	ds_read_b128 v[210:213], v222 offset:18432
	ds_read_b128 v[214:217], v222 offset:19456
	ds_read_b128 v[236:239], v222 offset:20480
	ds_read_b128 v[240:243], v222 offset:21504
	ds_read_b128 v[244:247], v222 offset:22528
	ds_read_b128 v[248:251], v222 offset:23552
	global_load_lds_dwordx4 v[194:195], off
	s_add_i32 m0, s65, 0x2000
	s_add_u32 s70, s40, 0x20000
	v_lshl_add_u64 v[196:197], s[40:41], 0, v[164:165]
	s_addc_u32 s71, s41, 0
	s_add_i32 s37, s37, s20
	global_load_lds_dwordx4 v[196:197], off
	v_lshl_add_u64 v[170:171], s[70:71], 0, v[162:163]
	s_mov_b32 m0, s37
	v_lshl_add_u64 v[198:199], s[68:69], 0, v[178:179]
	global_load_lds_dwordx4 v[170:171], off
	v_lshl_add_u64 v[170:171], s[70:71], 0, v[164:165]
	s_add_i32 m0, s37, 0x2000
	v_lshl_add_u64 v[200:201], s[68:69], 0, v[180:181]
	global_load_lds_dwordx4 v[170:171], off
	s_mov_b32 m0, s21
	s_nop 0
	global_load_lds_dwordx4 v[198:199], off
	s_mov_b32 m0, s22
	s_nop 0
	global_load_lds_dwordx4 v[200:201], off
	s_waitcnt vmcnt(8)
	s_waitcnt lgkmcnt(0)
	s_barrier
	s_setprio 1
	s_waitcnt lgkmcnt(0)
	v_mfma_scale_f32_16x16x128_f8f6f4 v[62:65], v[26:33], v[202:209], 0, v183, v169 op_sel_hi:[0,0,0]
	v_mfma_scale_f32_16x16x128_f8f6f4 v[58:61], v[18:25], v[202:209], 0, v183, v169 op_sel_hi:[0,0,0]
	v_mfma_scale_f32_16x16x128_f8f6f4 v[54:57], v[26:33], v[210:217], 0, v183, v169 op_sel_hi:[0,0,0]
	v_mfma_scale_f32_16x16x128_f8f6f4 v[50:53], v[18:25], v[210:217], 0, v183, v169 op_sel_hi:[0,0,0]
	v_mfma_scale_f32_16x16x128_f8f6f4 v[46:49], v[26:33], v[236:243], 0, v183, v169 op_sel_hi:[0,0,0]
	v_mfma_scale_f32_16x16x128_f8f6f4 v[42:45], v[18:25], v[236:243], 0, v183, v169 op_sel_hi:[0,0,0]
	v_mfma_scale_f32_16x16x128_f8f6f4 v[38:41], v[26:33], v[244:251], 0, v183, v169 op_sel_hi:[0,0,0]
	v_mfma_scale_f32_16x16x128_f8f6f4 v[34:37], v[18:25], v[244:251], 0, v183, v169 op_sel_hi:[0,0,0]
	s_setprio 0
	s_setprio 1
	v_mfma_scale_f32_16x16x128_f8f6f4 v[126:129], v[10:17], v[202:209], 0, v183, v169 op_sel_hi:[0,0,0]
	v_mfma_scale_f32_16x16x128_f8f6f4 v[122:125], v[2:9], v[202:209], 0, v183, v169 op_sel_hi:[0,0,0]
	v_mfma_scale_f32_16x16x128_f8f6f4 v[118:121], v[10:17], v[210:217], 0, v183, v169 op_sel_hi:[0,0,0]
	v_mfma_scale_f32_16x16x128_f8f6f4 v[114:117], v[2:9], v[210:217], 0, v183, v169 op_sel_hi:[0,0,0]
	v_mfma_scale_f32_16x16x128_f8f6f4 v[110:113], v[10:17], v[236:243], 0, v183, v169 op_sel_hi:[0,0,0]
	v_mfma_scale_f32_16x16x128_f8f6f4 v[106:109], v[2:9], v[236:243], 0, v183, v169 op_sel_hi:[0,0,0]
	v_mfma_scale_f32_16x16x128_f8f6f4 v[102:105], v[10:17], v[244:251], 0, v183, v169 op_sel_hi:[0,0,0]
	v_mfma_scale_f32_16x16x128_f8f6f4 v[98:101], v[2:9], v[244:251], 0, v183, v169 op_sel_hi:[0,0,0]
	s_setprio 0
	s_barrier
	s_add_i32 s37, 0, 0x18000
	s_add_i32 s65, 0, 0x1c000
	v_add_u32_e32 v2, s37, v221
	v_add_u32_e32 v6, s65, v221
	ds_read_b128 v[26:29], v2
	ds_read_b128 v[30:33], v2 offset:1024
	ds_read_b128 v[18:21], v2 offset:2048
	ds_read_b128 v[22:25], v2 offset:3072
	ds_read_b128 v[10:13], v6
	ds_read_b128 v[14:17], v6 offset:1024
	ds_read_b128 v[2:5], v6 offset:2048
	ds_read_b128 v[6:9], v6 offset:3072
	s_add_u32 s68, s68, 0x20000
	s_addc_u32 s69, s69, 0
	s_mov_b32 m0, s23
	v_lshl_add_u64 v[170:171], s[68:69], 0, v[178:179]
	ds_read_b128 v[202:205], v222 offset:32768
	ds_read_b128 v[206:209], v222 offset:33792
	ds_read_b128 v[210:213], v222 offset:34816
	ds_read_b128 v[214:217], v222 offset:35840
	ds_read_b128 v[236:239], v222 offset:36864
	ds_read_b128 v[240:243], v222 offset:37888
	ds_read_b128 v[244:247], v222 offset:38912
	ds_read_b128 v[248:251], v222 offset:39936
	global_load_lds_dwordx4 v[170:171], off
	v_lshl_add_u64 v[170:171], s[68:69], 0, v[180:181]
	s_mov_b32 m0, s12
	s_nop 0
	global_load_lds_dwordx4 v[170:171], off
	s_waitcnt vmcnt(8)
	s_waitcnt lgkmcnt(0)
	s_barrier
	s_setprio 1
	s_waitcnt lgkmcnt(0)
	v_mfma_scale_f32_16x16x128_f8f6f4 v[94:97], v[26:33], v[202:209], v[94:97], v183, v169 op_sel_hi:[0,0,0]
	v_mfma_scale_f32_16x16x128_f8f6f4 v[90:93], v[18:25], v[202:209], v[90:93], v183, v169 op_sel_hi:[0,0,0]
	v_mfma_scale_f32_16x16x128_f8f6f4 v[86:89], v[26:33], v[210:217], v[86:89], v183, v169 op_sel_hi:[0,0,0]
	v_mfma_scale_f32_16x16x128_f8f6f4 v[82:85], v[18:25], v[210:217], v[82:85], v183, v169 op_sel_hi:[0,0,0]
	v_mfma_scale_f32_16x16x128_f8f6f4 v[78:81], v[26:33], v[236:243], v[78:81], v183, v169 op_sel_hi:[0,0,0]
	v_mfma_scale_f32_16x16x128_f8f6f4 v[74:77], v[18:25], v[236:243], v[74:77], v183, v169 op_sel_hi:[0,0,0]
	v_mfma_scale_f32_16x16x128_f8f6f4 v[70:73], v[26:33], v[244:251], v[70:73], v183, v169 op_sel_hi:[0,0,0]
	v_mfma_scale_f32_16x16x128_f8f6f4 v[66:69], v[18:25], v[244:251], v[66:69], v183, v169 op_sel_hi:[0,0,0]
	s_setprio 0
	s_setprio 1
	v_mfma_scale_f32_16x16x128_f8f6f4 v[158:161], v[10:17], v[202:209], v[158:161], v183, v169 op_sel_hi:[0,0,0]
	v_mfma_scale_f32_16x16x128_f8f6f4 v[154:157], v[2:9], v[202:209], v[154:157], v183, v169 op_sel_hi:[0,0,0]
	v_mfma_scale_f32_16x16x128_f8f6f4 v[150:153], v[10:17], v[210:217], v[150:153], v183, v169 op_sel_hi:[0,0,0]
	v_mfma_scale_f32_16x16x128_f8f6f4 v[146:149], v[2:9], v[210:217], v[146:149], v183, v169 op_sel_hi:[0,0,0]
	v_mfma_scale_f32_16x16x128_f8f6f4 v[142:145], v[10:17], v[236:243], v[142:145], v183, v169 op_sel_hi:[0,0,0]
	v_mfma_scale_f32_16x16x128_f8f6f4 v[138:141], v[2:9], v[236:243], v[138:141], v183, v169 op_sel_hi:[0,0,0]
	v_mfma_scale_f32_16x16x128_f8f6f4 v[134:137], v[10:17], v[244:251], v[134:137], v183, v169 op_sel_hi:[0,0,0]
	v_mfma_scale_f32_16x16x128_f8f6f4 v[130:133], v[2:9], v[244:251], v[130:133], v183, v169 op_sel_hi:[0,0,0]
	s_setprio 0
	s_barrier
	s_add_i32 s37, s37, s20
	v_lshl_add_u64 v[170:171], v[194:195], 0, s[56:57]
	s_mov_b32 m0, s37
	ds_read_b128 v[202:205], v222 offset:49152
	ds_read_b128 v[206:209], v222 offset:50176
	ds_read_b128 v[210:213], v222 offset:51200
	ds_read_b128 v[214:217], v222 offset:52224
	ds_read_b128 v[236:239], v222 offset:53248
	ds_read_b128 v[240:243], v222 offset:54272
	ds_read_b128 v[244:247], v222 offset:55296
	ds_read_b128 v[248:251], v222 offset:56320
	global_load_lds_dwordx4 v[170:171], off
	s_add_i32 m0, s37, 0x2000
	s_add_u32 s40, s40, 0x20080
	v_lshl_add_u64 v[170:171], v[196:197], 0, s[56:57]
	s_addc_u32 s41, s41, 0
	s_add_i32 s37, s65, s20
	global_load_lds_dwordx4 v[170:171], off
	v_lshl_add_u64 v[170:171], s[40:41], 0, v[162:163]
	s_mov_b32 m0, s37
	s_nop 0
	global_load_lds_dwordx4 v[170:171], off
	v_lshl_add_u64 v[170:171], s[40:41], 0, v[164:165]
	s_add_i32 m0, s37, 0x2000
	s_nop 0
	global_load_lds_dwordx4 v[170:171], off
	v_lshl_add_u64 v[170:171], v[198:199], 0, s[56:57]
	s_mov_b32 m0, s92
	s_nop 0
	global_load_lds_dwordx4 v[170:171], off
	v_lshl_add_u64 v[170:171], v[200:201], 0, s[56:57]
	s_mov_b32 m0, s93
	s_nop 0
	global_load_lds_dwordx4 v[170:171], off
	s_waitcnt vmcnt(8)
	s_waitcnt lgkmcnt(0)
	s_barrier
	s_setprio 1
	s_waitcnt lgkmcnt(0)
	v_mfma_scale_f32_16x16x128_f8f6f4 v[62:65], v[26:33], v[202:209], v[62:65], v183, v169 op_sel_hi:[0,0,0]
	v_mfma_scale_f32_16x16x128_f8f6f4 v[58:61], v[18:25], v[202:209], v[58:61], v183, v169 op_sel_hi:[0,0,0]
	v_mfma_scale_f32_16x16x128_f8f6f4 v[54:57], v[26:33], v[210:217], v[54:57], v183, v169 op_sel_hi:[0,0,0]
	v_mfma_scale_f32_16x16x128_f8f6f4 v[50:53], v[18:25], v[210:217], v[50:53], v183, v169 op_sel_hi:[0,0,0]
	v_mfma_scale_f32_16x16x128_f8f6f4 v[46:49], v[26:33], v[236:243], v[46:49], v183, v169 op_sel_hi:[0,0,0]
	v_mfma_scale_f32_16x16x128_f8f6f4 v[42:45], v[18:25], v[236:243], v[42:45], v183, v169 op_sel_hi:[0,0,0]
	v_mfma_scale_f32_16x16x128_f8f6f4 v[38:41], v[26:33], v[244:251], v[38:41], v183, v169 op_sel_hi:[0,0,0]
	v_mfma_scale_f32_16x16x128_f8f6f4 v[34:37], v[18:25], v[244:251], v[34:37], v183, v169 op_sel_hi:[0,0,0]
	s_setprio 0
	s_setprio 1
	v_mfma_scale_f32_16x16x128_f8f6f4 v[126:129], v[10:17], v[202:209], v[126:129], v183, v169 op_sel_hi:[0,0,0]
	v_mfma_scale_f32_16x16x128_f8f6f4 v[122:125], v[2:9], v[202:209], v[122:125], v183, v169 op_sel_hi:[0,0,0]
	v_mfma_scale_f32_16x16x128_f8f6f4 v[118:121], v[10:17], v[210:217], v[118:121], v183, v169 op_sel_hi:[0,0,0]
	v_mfma_scale_f32_16x16x128_f8f6f4 v[114:117], v[2:9], v[210:217], v[114:117], v183, v169 op_sel_hi:[0,0,0]
	v_mfma_scale_f32_16x16x128_f8f6f4 v[110:113], v[10:17], v[236:243], v[110:113], v183, v169 op_sel_hi:[0,0,0]
	v_mfma_scale_f32_16x16x128_f8f6f4 v[106:109], v[2:9], v[236:243], v[106:109], v183, v169 op_sel_hi:[0,0,0]
	v_mfma_scale_f32_16x16x128_f8f6f4 v[102:105], v[10:17], v[244:251], v[102:105], v183, v169 op_sel_hi:[0,0,0]
	v_mfma_scale_f32_16x16x128_f8f6f4 v[98:101], v[2:9], v[244:251], v[98:101], v183, v169 op_sel_hi:[0,0,0]
	s_setprio 0
	s_barrier
	s_add_u32 s16, s16, 0x100
	s_addc_u32 s19, s19, 0
	s_add_u32 s38, s38, 0x100
	s_addc_u32 s39, s39, 0
	s_cmp_ge_i32 s27, s74
	s_mov_b32 s37, s27
	s_cbranch_scc0 .LBB0_1016
	s_branch .Lpeelexitph9

.Lpeelexitph9:
	s_mov_b64 s[70:71], 0xe800800
	v_mov_b32_e32 v209, v1
	s_and_b64 vcc, exec, s[52:53]
	s_cbranch_vccz .LBB0_1019

.Lpeelph15_1:
	s_add_i32 s91, s91, 2
	s_add_u32 s64, s70, 0x100
	s_addc_u32 s65, s71, 0
	s_and_b64 s[74:75], s[68:69], exec
	s_cselect_b32 s74, 0, s64
	s_cselect_b32 s75, 0, s65
	s_add_u32 s74, s28, s74
	s_addc_u32 s75, s29, s75
	s_add_u32 s92, s51, s70
	s_addc_u32 s93, s53, s71
	s_and_b64 s[68:69], s[68:69], exec
	s_cselect_b32 s69, s55, s93
	s_cselect_b32 s68, s54, s92
	s_add_i32 s93, 0, 0x10000
	s_add_i32 s92, 0, 0x14000
	v_add_u32_e32 v2, s93, v210
	v_add_u32_e32 v6, s92, v210
	ds_read_b128 v[26:29], v2
	ds_read_b128 v[30:33], v2 offset:1024
	ds_read_b128 v[18:21], v2 offset:2048
	ds_read_b128 v[22:25], v2 offset:3072
	ds_read_b128 v[10:13], v6
	ds_read_b128 v[14:17], v6 offset:1024
	ds_read_b128 v[2:5], v6 offset:2048
	ds_read_b128 v[6:9], v6 offset:3072
	v_lshl_add_u64 v[170:171], v[194:195], 0, s[70:71]
	s_add_i32 m0, s59, 0xc000
	ds_read_b128 v[196:199], v212
	ds_read_b128 v[200:203], v212 offset:1024
	ds_read_b128 v[214:217], v212 offset:2048
	ds_read_b128 v[218:221], v212 offset:3072
	ds_read_b128 v[236:239], v212 offset:4096
	ds_read_b128 v[240:243], v212 offset:5120
	ds_read_b128 v[244:247], v212 offset:6144
	ds_read_b128 v[248:251], v212 offset:7168
	global_load_lds_dwordx4 v[170:171], off
	v_lshl_add_u64 v[170:171], v[192:193], 0, s[70:71]
	s_add_i32 m0, s59, 0xe000
	s_nop 0
	global_load_lds_dwordx4 v[170:171], off
	s_waitcnt vmcnt(8)
	s_waitcnt lgkmcnt(0)
	s_barrier
	s_setprio 1
	s_waitcnt lgkmcnt(0)
	v_mfma_scale_f32_16x16x128_f8f6f4 v[154:157], v[26:33], v[196:203], 0, v208, v207 op_sel_hi:[0,0,0]
	v_mfma_scale_f32_16x16x128_f8f6f4 v[150:153], v[18:25], v[196:203], 0, v208, v207 op_sel_hi:[0,0,0]
	v_mfma_scale_f32_16x16x128_f8f6f4 v[142:145], v[26:33], v[214:221], 0, v208, v207 op_sel_hi:[0,0,0]
	v_mfma_scale_f32_16x16x128_f8f6f4 v[134:137], v[18:25], v[214:221], 0, v208, v207 op_sel_hi:[0,0,0]
	v_mfma_scale_f32_16x16x128_f8f6f4 v[126:129], v[26:33], v[236:243], 0, v208, v207 op_sel_hi:[0,0,0]
	v_mfma_scale_f32_16x16x128_f8f6f4 v[118:121], v[18:25], v[236:243], 0, v208, v207 op_sel_hi:[0,0,0]
	v_mfma_scale_f32_16x16x128_f8f6f4 v[110:113], v[26:33], v[244:251], 0, v208, v207 op_sel_hi:[0,0,0]
	v_mfma_scale_f32_16x16x128_f8f6f4 v[102:105], v[18:25], v[244:251], 0, v208, v207 op_sel_hi:[0,0,0]
	s_setprio 0
	s_setprio 1
	v_mfma_scale_f32_16x16x128_f8f6f4 v[158:161], v[10:17], v[196:203], 0, v208, v207 op_sel_hi:[0,0,0]
	v_mfma_scale_f32_16x16x128_f8f6f4 v[146:149], v[2:9], v[196:203], 0, v208, v207 op_sel_hi:[0,0,0]
	v_mfma_scale_f32_16x16x128_f8f6f4 v[138:141], v[10:17], v[214:221], 0, v208, v207 op_sel_hi:[0,0,0]
	v_mfma_scale_f32_16x16x128_f8f6f4 v[130:133], v[2:9], v[214:221], 0, v208, v207 op_sel_hi:[0,0,0]
	v_mfma_scale_f32_16x16x128_f8f6f4 v[122:125], v[10:17], v[236:243], 0, v208, v207 op_sel_hi:[0,0,0]
	v_mfma_scale_f32_16x16x128_f8f6f4 v[114:117], v[2:9], v[236:243], 0, v208, v207 op_sel_hi:[0,0,0]
	v_mfma_scale_f32_16x16x128_f8f6f4 v[106:109], v[10:17], v[244:251], 0, v208, v207 op_sel_hi:[0,0,0]
	v_mfma_scale_f32_16x16x128_f8f6f4 v[98:101], v[2:9], v[244:251], 0, v208, v207 op_sel_hi:[0,0,0]
	s_setprio 0
	s_barrier
	s_add_i32 s70, s93, s72
	v_lshl_add_u64 v[196:197], s[68:69], 0, v[162:163]
	s_mov_b32 m0, s70
	ds_read_b128 v[214:217], v212 offset:16384
	ds_read_b128 v[218:221], v212 offset:17408
	ds_read_b128 v[236:239], v212 offset:18432
	ds_read_b128 v[240:243], v212 offset:19456
	ds_read_b128 v[244:247], v212 offset:20480
	ds_read_b128 v[248:251], v212 offset:21504
	ds_read_b128 v[170:173], v212 offset:22528
	ds_read_b128 v[174:177], v212 offset:23552
	global_load_lds_dwordx4 v[196:197], off
	s_add_i32 m0, s70, 0x2000
	s_add_u32 s70, s68, 0x20000
	v_lshl_add_u64 v[198:199], s[68:69], 0, v[164:165]
	s_addc_u32 s71, s69, 0
	s_add_i32 s92, s92, s72
	global_load_lds_dwordx4 v[198:199], off
	v_lshl_add_u64 v[200:201], s[70:71], 0, v[162:163]
	s_mov_b32 m0, s92
	v_mov_b32_e32 v179, v167
	global_load_lds_dwordx4 v[200:201], off
	v_lshl_add_u64 v[200:201], s[70:71], 0, v[164:165]
	s_add_i32 m0, s92, 0x2000
	v_lshl_add_u64 v[202:203], s[74:75], 0, v[166:167]
	global_load_lds_dwordx4 v[200:201], off
	s_mov_b32 m0, s59
	v_lshl_add_u64 v[200:201], s[74:75], 0, v[178:179]
	global_load_lds_dwordx4 v166, s[74:75]
	s_mov_b32 m0, s61
	s_nop 0
	global_load_lds_dwordx4 v178, s[74:75]
	s_waitcnt vmcnt(8)
	s_waitcnt lgkmcnt(0)
	s_barrier
	s_setprio 1
	s_waitcnt lgkmcnt(0)
	v_mfma_scale_f32_16x16x128_f8f6f4 v[94:97], v[26:33], v[214:221], 0, v208, v207 op_sel_hi:[0,0,0]
	v_mfma_scale_f32_16x16x128_f8f6f4 v[86:89], v[18:25], v[214:221], 0, v208, v207 op_sel_hi:[0,0,0]
	v_mfma_scale_f32_16x16x128_f8f6f4 v[78:81], v[26:33], v[236:243], 0, v208, v207 op_sel_hi:[0,0,0]
	v_mfma_scale_f32_16x16x128_f8f6f4 v[70:73], v[18:25], v[236:243], 0, v208, v207 op_sel_hi:[0,0,0]
	v_mfma_scale_f32_16x16x128_f8f6f4 v[62:65], v[26:33], v[244:251], 0, v208, v207 op_sel_hi:[0,0,0]
	v_mfma_scale_f32_16x16x128_f8f6f4 v[54:57], v[18:25], v[244:251], 0, v208, v207 op_sel_hi:[0,0,0]
	v_mfma_scale_f32_16x16x128_f8f6f4 v[46:49], v[26:33], v[170:177], 0, v208, v207 op_sel_hi:[0,0,0]
	v_mfma_scale_f32_16x16x128_f8f6f4 v[38:41], v[18:25], v[170:177], 0, v208, v207 op_sel_hi:[0,0,0]
	s_setprio 0
	s_setprio 1
	v_mfma_scale_f32_16x16x128_f8f6f4 v[90:93], v[10:17], v[214:221], 0, v208, v207 op_sel_hi:[0,0,0]
	v_mfma_scale_f32_16x16x128_f8f6f4 v[82:85], v[2:9], v[214:221], 0, v208, v207 op_sel_hi:[0,0,0]
	v_mfma_scale_f32_16x16x128_f8f6f4 v[74:77], v[10:17], v[236:243], 0, v208, v207 op_sel_hi:[0,0,0]
	v_mfma_scale_f32_16x16x128_f8f6f4 v[66:69], v[2:9], v[236:243], 0, v208, v207 op_sel_hi:[0,0,0]
	v_mfma_scale_f32_16x16x128_f8f6f4 v[58:61], v[10:17], v[244:251], 0, v208, v207 op_sel_hi:[0,0,0]
	v_mfma_scale_f32_16x16x128_f8f6f4 v[50:53], v[2:9], v[244:251], 0, v208, v207 op_sel_hi:[0,0,0]
	v_mfma_scale_f32_16x16x128_f8f6f4 v[42:45], v[10:17], v[170:177], 0, v208, v207 op_sel_hi:[0,0,0]
	v_mfma_scale_f32_16x16x128_f8f6f4 v[34:37], v[2:9], v[170:177], 0, v208, v207 op_sel_hi:[0,0,0]
	s_setprio 0
	s_barrier
	s_add_i32 s70, 0, 0x18000
	s_add_i32 s71, 0, 0x1c000
	v_add_u32_e32 v2, s70, v210
	v_add_u32_e32 v6, s71, v210
	ds_read_b128 v[26:29], v2
	ds_read_b128 v[30:33], v2 offset:1024
	ds_read_b128 v[18:21], v2 offset:2048
	ds_read_b128 v[22:25], v2 offset:3072
	ds_read_b128 v[10:13], v6
	ds_read_b128 v[14:17], v6 offset:1024
	ds_read_b128 v[2:5], v6 offset:2048
	ds_read_b128 v[6:9], v6 offset:3072
	s_mov_b32 m0, s73
	ds_read_b128 v[170:173], v212 offset:32768
	ds_read_b128 v[174:177], v212 offset:33792
	ds_read_b128 v[214:217], v212 offset:34816
	ds_read_b128 v[218:221], v212 offset:35840
	ds_read_b128 v[236:239], v212 offset:36864
	ds_read_b128 v[240:243], v212 offset:37888
	ds_read_b128 v[244:247], v212 offset:38912
	ds_read_b128 v[248:251], v212 offset:39936
	global_load_lds_dwordx4 v180, s[74:75]
	s_mov_b32 m0, s76
	s_nop 0
	global_load_lds_dwordx4 v182, s[74:75]
	s_waitcnt vmcnt(8)
	s_waitcnt lgkmcnt(0)
	s_barrier
	s_setprio 1
	s_waitcnt lgkmcnt(0)
	v_mfma_scale_f32_16x16x128_f8f6f4 v[154:157], v[26:33], v[170:177], v[154:157], v208, v207 op_sel_hi:[0,0,0]
	v_mfma_scale_f32_16x16x128_f8f6f4 v[150:153], v[18:25], v[170:177], v[150:153], v208, v207 op_sel_hi:[0,0,0]
	v_mfma_scale_f32_16x16x128_f8f6f4 v[142:145], v[26:33], v[214:221], v[142:145], v208, v207 op_sel_hi:[0,0,0]
	v_mfma_scale_f32_16x16x128_f8f6f4 v[134:137], v[18:25], v[214:221], v[134:137], v208, v207 op_sel_hi:[0,0,0]
	v_mfma_scale_f32_16x16x128_f8f6f4 v[126:129], v[26:33], v[236:243], v[126:129], v208, v207 op_sel_hi:[0,0,0]
	v_mfma_scale_f32_16x16x128_f8f6f4 v[118:121], v[18:25], v[236:243], v[118:121], v208, v207 op_sel_hi:[0,0,0]
	v_mfma_scale_f32_16x16x128_f8f6f4 v[110:113], v[26:33], v[244:251], v[110:113], v208, v207 op_sel_hi:[0,0,0]
	v_mfma_scale_f32_16x16x128_f8f6f4 v[102:105], v[18:25], v[244:251], v[102:105], v208, v207 op_sel_hi:[0,0,0]
	s_setprio 0
	s_setprio 1
	v_mfma_scale_f32_16x16x128_f8f6f4 v[158:161], v[10:17], v[170:177], v[158:161], v208, v207 op_sel_hi:[0,0,0]
	v_mfma_scale_f32_16x16x128_f8f6f4 v[146:149], v[2:9], v[170:177], v[146:149], v208, v207 op_sel_hi:[0,0,0]
	v_mfma_scale_f32_16x16x128_f8f6f4 v[138:141], v[10:17], v[214:221], v[138:141], v208, v207 op_sel_hi:[0,0,0]
	v_mfma_scale_f32_16x16x128_f8f6f4 v[130:133], v[2:9], v[214:221], v[130:133], v208, v207 op_sel_hi:[0,0,0]
	v_mfma_scale_f32_16x16x128_f8f6f4 v[122:125], v[10:17], v[236:243], v[122:125], v208, v207 op_sel_hi:[0,0,0]
	v_mfma_scale_f32_16x16x128_f8f6f4 v[114:117], v[2:9], v[236:243], v[114:117], v208, v207 op_sel_hi:[0,0,0]
	v_mfma_scale_f32_16x16x128_f8f6f4 v[106:109], v[10:17], v[244:251], v[106:109], v208, v207 op_sel_hi:[0,0,0]
	v_mfma_scale_f32_16x16x128_f8f6f4 v[98:101], v[2:9], v[244:251], v[98:101], v208, v207 op_sel_hi:[0,0,0]
	s_setprio 0
	s_barrier
	s_add_i32 s70, s70, s72
	v_lshl_add_u64 v[196:197], v[196:197], 0, s[56:57]
	s_mov_b32 m0, s70
	ds_read_b128 v[170:173], v212 offset:49152
	ds_read_b128 v[174:177], v212 offset:50176
	ds_read_b128 v[214:217], v212 offset:51200
	ds_read_b128 v[218:221], v212 offset:52224
	ds_read_b128 v[236:239], v212 offset:53248
	ds_read_b128 v[240:243], v212 offset:54272
	ds_read_b128 v[244:247], v212 offset:55296
	ds_read_b128 v[248:251], v212 offset:56320
	global_load_lds_dwordx4 v[196:197], off
	s_add_i32 m0, s70, 0x2000
	s_add_u32 s68, s68, 0x20080
	v_lshl_add_u64 v[196:197], v[198:199], 0, s[56:57]
	s_addc_u32 s69, s69, 0
	s_add_i32 s70, s71, s72
	global_load_lds_dwordx4 v[196:197], off
	v_lshl_add_u64 v[196:197], s[68:69], 0, v[162:163]
	s_mov_b32 m0, s70
	s_nop 0
	global_load_lds_dwordx4 v[196:197], off
	v_lshl_add_u64 v[196:197], s[68:69], 0, v[164:165]
	s_add_i32 m0, s70, 0x2000
	s_nop 0
	global_load_lds_dwordx4 v[196:197], off
	v_lshl_add_u64 v[196:197], v[202:203], 0, s[56:57]
	s_mov_b32 m0, s77
	s_nop 0
	global_load_lds_dwordx4 v[196:197], off
	v_lshl_add_u64 v[196:197], v[200:201], 0, s[56:57]
	s_mov_b32 m0, s79
	s_nop 0
	global_load_lds_dwordx4 v[196:197], off
	s_waitcnt vmcnt(8)
	s_waitcnt lgkmcnt(0)
	s_barrier
	s_setprio 1
	s_waitcnt lgkmcnt(0)
	v_mfma_scale_f32_16x16x128_f8f6f4 v[94:97], v[26:33], v[170:177], v[94:97], v208, v207 op_sel_hi:[0,0,0]
	v_mfma_scale_f32_16x16x128_f8f6f4 v[86:89], v[18:25], v[170:177], v[86:89], v208, v207 op_sel_hi:[0,0,0]
	v_mfma_scale_f32_16x16x128_f8f6f4 v[78:81], v[26:33], v[214:221], v[78:81], v208, v207 op_sel_hi:[0,0,0]
	v_mfma_scale_f32_16x16x128_f8f6f4 v[70:73], v[18:25], v[214:221], v[70:73], v208, v207 op_sel_hi:[0,0,0]
	v_mfma_scale_f32_16x16x128_f8f6f4 v[62:65], v[26:33], v[236:243], v[62:65], v208, v207 op_sel_hi:[0,0,0]
	v_mfma_scale_f32_16x16x128_f8f6f4 v[54:57], v[18:25], v[236:243], v[54:57], v208, v207 op_sel_hi:[0,0,0]
	v_mfma_scale_f32_16x16x128_f8f6f4 v[46:49], v[26:33], v[244:251], v[46:49], v208, v207 op_sel_hi:[0,0,0]
	v_mfma_scale_f32_16x16x128_f8f6f4 v[38:41], v[18:25], v[244:251], v[38:41], v208, v207 op_sel_hi:[0,0,0]
	s_setprio 0
	s_setprio 1
	v_mfma_scale_f32_16x16x128_f8f6f4 v[90:93], v[10:17], v[170:177], v[90:93], v208, v207 op_sel_hi:[0,0,0]
	v_mfma_scale_f32_16x16x128_f8f6f4 v[82:85], v[2:9], v[170:177], v[82:85], v208, v207 op_sel_hi:[0,0,0]
	v_mfma_scale_f32_16x16x128_f8f6f4 v[74:77], v[10:17], v[214:221], v[74:77], v208, v207 op_sel_hi:[0,0,0]
	v_mfma_scale_f32_16x16x128_f8f6f4 v[66:69], v[2:9], v[214:221], v[66:69], v208, v207 op_sel_hi:[0,0,0]
	v_mfma_scale_f32_16x16x128_f8f6f4 v[58:61], v[10:17], v[236:243], v[58:61], v208, v207 op_sel_hi:[0,0,0]
	v_mfma_scale_f32_16x16x128_f8f6f4 v[50:53], v[2:9], v[236:243], v[50:53], v208, v207 op_sel_hi:[0,0,0]
	v_mfma_scale_f32_16x16x128_f8f6f4 v[42:45], v[10:17], v[244:251], v[42:45], v208, v207 op_sel_hi:[0,0,0]
	v_mfma_scale_f32_16x16x128_f8f6f4 v[34:37], v[2:9], v[244:251], v[34:37], v208, v207 op_sel_hi:[0,0,0]
	s_setprio 0
	s_barrier
	s_cmp_ge_i32 s91, s11
	s_cbranch_scc1 .LBB0_1695
	s_mov_b64 s[70:71], s[64:65]
	s_branch .LBB0_1691

.Lpeelph17_1:
	s_add_i32 s55, s55, 2
	s_add_u32 s60, s64, 0x100
	s_addc_u32 s61, s65, 0
	s_and_b64 s[68:69], s[62:63], exec
	s_cselect_b32 s68, 0, s60
	s_cselect_b32 s69, 0, s61
	s_add_u32 s68, s30, s68
	s_addc_u32 s69, s31, s69
	s_add_u32 s91, s47, s64
	s_addc_u32 s92, s49, s65
	s_and_b64 s[62:63], s[62:63], exec
	s_cselect_b32 s63, s53, s92
	s_cselect_b32 s62, s52, s91
	s_add_i32 s92, 0, 0x10000
	s_add_i32 s91, 0, 0x14000
	v_add_u32_e32 v2, s92, v210
	v_add_u32_e32 v6, s91, v210
	ds_read_b128 v[26:29], v2
	ds_read_b128 v[30:33], v2 offset:1024
	ds_read_b128 v[18:21], v2 offset:2048
	ds_read_b128 v[22:25], v2 offset:3072
	ds_read_b128 v[10:13], v6
	ds_read_b128 v[14:17], v6 offset:1024
	ds_read_b128 v[2:5], v6 offset:2048
	ds_read_b128 v[6:9], v6 offset:3072
	v_lshl_add_u64 v[222:223], v[194:195], 0, s[64:65]
	s_add_i32 m0, s59, 0xc000
	ds_read_b128 v[170:173], v212
	ds_read_b128 v[174:177], v212 offset:1024
	ds_read_b128 v[196:199], v212 offset:2048
	ds_read_b128 v[200:203], v212 offset:3072
	ds_read_b128 v[214:217], v212 offset:4096
	ds_read_b128 v[218:221], v212 offset:5120
	ds_read_b128 v[236:239], v212 offset:6144
	ds_read_b128 v[240:243], v212 offset:7168
	global_load_lds_dwordx4 v[222:223], off
	v_lshl_add_u64 v[222:223], v[192:193], 0, s[64:65]
	s_add_i32 m0, s59, 0xe000
	s_nop 0
	global_load_lds_dwordx4 v[222:223], off
	s_waitcnt vmcnt(8)
	s_waitcnt lgkmcnt(0)
	s_barrier
	s_setprio 1
	s_waitcnt lgkmcnt(0)
	v_mfma_scale_f32_16x16x128_f8f6f4 v[154:157], v[26:33], v[170:177], 0, v208, v207 op_sel_hi:[0,0,0]
	v_mfma_scale_f32_16x16x128_f8f6f4 v[150:153], v[18:25], v[170:177], 0, v208, v207 op_sel_hi:[0,0,0]
	v_mfma_scale_f32_16x16x128_f8f6f4 v[142:145], v[26:33], v[196:203], 0, v208, v207 op_sel_hi:[0,0,0]
	v_mfma_scale_f32_16x16x128_f8f6f4 v[134:137], v[18:25], v[196:203], 0, v208, v207 op_sel_hi:[0,0,0]
	v_mfma_scale_f32_16x16x128_f8f6f4 v[126:129], v[26:33], v[214:221], 0, v208, v207 op_sel_hi:[0,0,0]
	v_mfma_scale_f32_16x16x128_f8f6f4 v[118:121], v[18:25], v[214:221], 0, v208, v207 op_sel_hi:[0,0,0]
	v_mfma_scale_f32_16x16x128_f8f6f4 v[110:113], v[26:33], v[236:243], 0, v208, v207 op_sel_hi:[0,0,0]
	v_mfma_scale_f32_16x16x128_f8f6f4 v[102:105], v[18:25], v[236:243], 0, v208, v207 op_sel_hi:[0,0,0]
	s_setprio 0
	s_setprio 1
	v_mfma_scale_f32_16x16x128_f8f6f4 v[158:161], v[10:17], v[170:177], 0, v208, v207 op_sel_hi:[0,0,0]
	v_mfma_scale_f32_16x16x128_f8f6f4 v[146:149], v[2:9], v[170:177], 0, v208, v207 op_sel_hi:[0,0,0]
	v_mfma_scale_f32_16x16x128_f8f6f4 v[138:141], v[10:17], v[196:203], 0, v208, v207 op_sel_hi:[0,0,0]
	v_mfma_scale_f32_16x16x128_f8f6f4 v[130:133], v[2:9], v[196:203], 0, v208, v207 op_sel_hi:[0,0,0]
	v_mfma_scale_f32_16x16x128_f8f6f4 v[122:125], v[10:17], v[214:221], 0, v208, v207 op_sel_hi:[0,0,0]
	v_mfma_scale_f32_16x16x128_f8f6f4 v[114:117], v[2:9], v[214:221], 0, v208, v207 op_sel_hi:[0,0,0]
	v_mfma_scale_f32_16x16x128_f8f6f4 v[106:109], v[10:17], v[236:243], 0, v208, v207 op_sel_hi:[0,0,0]
	v_mfma_scale_f32_16x16x128_f8f6f4 v[98:101], v[2:9], v[236:243], 0, v208, v207 op_sel_hi:[0,0,0]
	s_setprio 0
	s_barrier
	s_add_i32 s64, s92, s22
	v_lshl_add_u64 v[196:197], s[62:63], 0, v[162:163]
	s_mov_b32 m0, s64
	ds_read_b128 v[170:173], v212 offset:16384
	ds_read_b128 v[174:177], v212 offset:17408
	ds_read_b128 v[214:217], v212 offset:18432
	ds_read_b128 v[218:221], v212 offset:19456
	ds_read_b128 v[236:239], v212 offset:20480
	ds_read_b128 v[240:243], v212 offset:21504
	ds_read_b128 v[244:247], v212 offset:22528
	ds_read_b128 v[248:251], v212 offset:23552
	global_load_lds_dwordx4 v[196:197], off
	s_add_i32 m0, s64, 0x2000
	s_add_u32 s64, s62, 0x20000
	v_lshl_add_u64 v[198:199], s[62:63], 0, v[164:165]
	s_addc_u32 s65, s63, 0
	s_add_i32 s91, s91, s22
	global_load_lds_dwordx4 v[198:199], off
	v_lshl_add_u64 v[200:201], s[64:65], 0, v[162:163]
	s_mov_b32 m0, s91
	v_mov_b32_e32 v179, v167
	global_load_lds_dwordx4 v[200:201], off
	v_lshl_add_u64 v[200:201], s[64:65], 0, v[164:165]
	s_add_i32 m0, s91, 0x2000
	v_lshl_add_u64 v[202:203], s[68:69], 0, v[166:167]
	global_load_lds_dwordx4 v[200:201], off
	s_mov_b32 m0, s59
	v_lshl_add_u64 v[200:201], s[68:69], 0, v[178:179]
	global_load_lds_dwordx4 v166, s[68:69]
	s_mov_b32 m0, s71
	s_nop 0
	global_load_lds_dwordx4 v178, s[68:69]
	s_waitcnt vmcnt(8)
	s_waitcnt lgkmcnt(0)
	s_barrier
	s_setprio 1
	s_waitcnt lgkmcnt(0)
	v_mfma_scale_f32_16x16x128_f8f6f4 v[94:97], v[26:33], v[170:177], 0, v208, v207 op_sel_hi:[0,0,0]
	v_mfma_scale_f32_16x16x128_f8f6f4 v[86:89], v[18:25], v[170:177], 0, v208, v207 op_sel_hi:[0,0,0]
	v_mfma_scale_f32_16x16x128_f8f6f4 v[78:81], v[26:33], v[214:221], 0, v208, v207 op_sel_hi:[0,0,0]
	v_mfma_scale_f32_16x16x128_f8f6f4 v[70:73], v[18:25], v[214:221], 0, v208, v207 op_sel_hi:[0,0,0]
	v_mfma_scale_f32_16x16x128_f8f6f4 v[62:65], v[26:33], v[236:243], 0, v208, v207 op_sel_hi:[0,0,0]
	v_mfma_scale_f32_16x16x128_f8f6f4 v[54:57], v[18:25], v[236:243], 0, v208, v207 op_sel_hi:[0,0,0]
	v_mfma_scale_f32_16x16x128_f8f6f4 v[46:49], v[26:33], v[244:251], 0, v208, v207 op_sel_hi:[0,0,0]
	v_mfma_scale_f32_16x16x128_f8f6f4 v[38:41], v[18:25], v[244:251], 0, v208, v207 op_sel_hi:[0,0,0]
	s_setprio 0
	s_setprio 1
	v_mfma_scale_f32_16x16x128_f8f6f4 v[90:93], v[10:17], v[170:177], 0, v208, v207 op_sel_hi:[0,0,0]
	v_mfma_scale_f32_16x16x128_f8f6f4 v[82:85], v[2:9], v[170:177], 0, v208, v207 op_sel_hi:[0,0,0]
	v_mfma_scale_f32_16x16x128_f8f6f4 v[74:77], v[10:17], v[214:221], 0, v208, v207 op_sel_hi:[0,0,0]
	v_mfma_scale_f32_16x16x128_f8f6f4 v[66:69], v[2:9], v[214:221], 0, v208, v207 op_sel_hi:[0,0,0]
	v_mfma_scale_f32_16x16x128_f8f6f4 v[58:61], v[10:17], v[236:243], 0, v208, v207 op_sel_hi:[0,0,0]
	v_mfma_scale_f32_16x16x128_f8f6f4 v[50:53], v[2:9], v[236:243], 0, v208, v207 op_sel_hi:[0,0,0]
	v_mfma_scale_f32_16x16x128_f8f6f4 v[42:45], v[10:17], v[244:251], 0, v208, v207 op_sel_hi:[0,0,0]
	v_mfma_scale_f32_16x16x128_f8f6f4 v[34:37], v[2:9], v[244:251], 0, v208, v207 op_sel_hi:[0,0,0]
	s_setprio 0
	s_barrier
	s_add_i32 s64, 0, 0x18000
	s_add_i32 s65, 0, 0x1c000
	v_add_u32_e32 v2, s64, v210
	v_add_u32_e32 v6, s65, v210
	ds_read_b128 v[26:29], v2
	ds_read_b128 v[30:33], v2 offset:1024
	ds_read_b128 v[18:21], v2 offset:2048
	ds_read_b128 v[22:25], v2 offset:3072
	ds_read_b128 v[10:13], v6
	ds_read_b128 v[14:17], v6 offset:1024
	ds_read_b128 v[2:5], v6 offset:2048
	ds_read_b128 v[6:9], v6 offset:3072
	s_mov_b32 m0, s72
	ds_read_b128 v[170:173], v212 offset:32768
	ds_read_b128 v[174:177], v212 offset:33792
	ds_read_b128 v[214:217], v212 offset:34816
	ds_read_b128 v[218:221], v212 offset:35840
	ds_read_b128 v[236:239], v212 offset:36864
	ds_read_b128 v[240:243], v212 offset:37888
	ds_read_b128 v[244:247], v212 offset:38912
	ds_read_b128 v[248:251], v212 offset:39936
	global_load_lds_dwordx4 v180, s[68:69]
	s_mov_b32 m0, s73
	s_nop 0
	global_load_lds_dwordx4 v182, s[68:69]
	s_waitcnt vmcnt(8)
	s_waitcnt lgkmcnt(0)
	s_barrier
	s_setprio 1
	s_waitcnt lgkmcnt(0)
	v_mfma_scale_f32_16x16x128_f8f6f4 v[154:157], v[26:33], v[170:177], v[154:157], v208, v207 op_sel_hi:[0,0,0]
	v_mfma_scale_f32_16x16x128_f8f6f4 v[150:153], v[18:25], v[170:177], v[150:153], v208, v207 op_sel_hi:[0,0,0]
	v_mfma_scale_f32_16x16x128_f8f6f4 v[142:145], v[26:33], v[214:221], v[142:145], v208, v207 op_sel_hi:[0,0,0]
	v_mfma_scale_f32_16x16x128_f8f6f4 v[134:137], v[18:25], v[214:221], v[134:137], v208, v207 op_sel_hi:[0,0,0]
	v_mfma_scale_f32_16x16x128_f8f6f4 v[126:129], v[26:33], v[236:243], v[126:129], v208, v207 op_sel_hi:[0,0,0]
	v_mfma_scale_f32_16x16x128_f8f6f4 v[118:121], v[18:25], v[236:243], v[118:121], v208, v207 op_sel_hi:[0,0,0]
	v_mfma_scale_f32_16x16x128_f8f6f4 v[110:113], v[26:33], v[244:251], v[110:113], v208, v207 op_sel_hi:[0,0,0]
	v_mfma_scale_f32_16x16x128_f8f6f4 v[102:105], v[18:25], v[244:251], v[102:105], v208, v207 op_sel_hi:[0,0,0]
	s_setprio 0
	s_setprio 1
	v_mfma_scale_f32_16x16x128_f8f6f4 v[158:161], v[10:17], v[170:177], v[158:161], v208, v207 op_sel_hi:[0,0,0]
	v_mfma_scale_f32_16x16x128_f8f6f4 v[146:149], v[2:9], v[170:177], v[146:149], v208, v207 op_sel_hi:[0,0,0]
	v_mfma_scale_f32_16x16x128_f8f6f4 v[138:141], v[10:17], v[214:221], v[138:141], v208, v207 op_sel_hi:[0,0,0]
	v_mfma_scale_f32_16x16x128_f8f6f4 v[130:133], v[2:9], v[214:221], v[130:133], v208, v207 op_sel_hi:[0,0,0]
	v_mfma_scale_f32_16x16x128_f8f6f4 v[122:125], v[10:17], v[236:243], v[122:125], v208, v207 op_sel_hi:[0,0,0]
	v_mfma_scale_f32_16x16x128_f8f6f4 v[114:117], v[2:9], v[236:243], v[114:117], v208, v207 op_sel_hi:[0,0,0]
	v_mfma_scale_f32_16x16x128_f8f6f4 v[106:109], v[10:17], v[244:251], v[106:109], v208, v207 op_sel_hi:[0,0,0]
	v_mfma_scale_f32_16x16x128_f8f6f4 v[98:101], v[2:9], v[244:251], v[98:101], v208, v207 op_sel_hi:[0,0,0]
	s_setprio 0
	s_barrier
	s_add_i32 s64, s64, s22
	v_lshl_add_u64 v[196:197], v[196:197], 0, s[56:57]
	s_mov_b32 m0, s64
	ds_read_b128 v[170:173], v212 offset:49152
	ds_read_b128 v[174:177], v212 offset:50176
	ds_read_b128 v[214:217], v212 offset:51200
	ds_read_b128 v[218:221], v212 offset:52224
	ds_read_b128 v[236:239], v212 offset:53248
	ds_read_b128 v[240:243], v212 offset:54272
	ds_read_b128 v[244:247], v212 offset:55296
	ds_read_b128 v[248:251], v212 offset:56320
	global_load_lds_dwordx4 v[196:197], off
	s_add_i32 m0, s64, 0x2000
	s_add_u32 s62, s62, 0x20080
	v_lshl_add_u64 v[196:197], v[198:199], 0, s[56:57]
	s_addc_u32 s63, s63, 0
	s_add_i32 s64, s65, s22
	global_load_lds_dwordx4 v[196:197], off
	v_lshl_add_u64 v[196:197], s[62:63], 0, v[162:163]
	s_mov_b32 m0, s64
	s_nop 0
	global_load_lds_dwordx4 v[196:197], off
	v_lshl_add_u64 v[196:197], s[62:63], 0, v[164:165]
	s_add_i32 m0, s64, 0x2000
	s_nop 0
	global_load_lds_dwordx4 v[196:197], off
	v_lshl_add_u64 v[196:197], v[202:203], 0, s[56:57]
	s_mov_b32 m0, s74
	s_nop 0
	global_load_lds_dwordx4 v[196:197], off
	v_lshl_add_u64 v[196:197], v[200:201], 0, s[56:57]
	s_mov_b32 m0, s75
	s_nop 0
	global_load_lds_dwordx4 v[196:197], off
	s_waitcnt vmcnt(8)
	s_waitcnt lgkmcnt(0)
	s_barrier
	s_setprio 1
	s_waitcnt lgkmcnt(0)
	v_mfma_scale_f32_16x16x128_f8f6f4 v[94:97], v[26:33], v[170:177], v[94:97], v208, v207 op_sel_hi:[0,0,0]
	v_mfma_scale_f32_16x16x128_f8f6f4 v[86:89], v[18:25], v[170:177], v[86:89], v208, v207 op_sel_hi:[0,0,0]
	v_mfma_scale_f32_16x16x128_f8f6f4 v[78:81], v[26:33], v[214:221], v[78:81], v208, v207 op_sel_hi:[0,0,0]
	v_mfma_scale_f32_16x16x128_f8f6f4 v[70:73], v[18:25], v[214:221], v[70:73], v208, v207 op_sel_hi:[0,0,0]
	v_mfma_scale_f32_16x16x128_f8f6f4 v[62:65], v[26:33], v[236:243], v[62:65], v208, v207 op_sel_hi:[0,0,0]
	v_mfma_scale_f32_16x16x128_f8f6f4 v[54:57], v[18:25], v[236:243], v[54:57], v208, v207 op_sel_hi:[0,0,0]
	v_mfma_scale_f32_16x16x128_f8f6f4 v[46:49], v[26:33], v[244:251], v[46:49], v208, v207 op_sel_hi:[0,0,0]
	v_mfma_scale_f32_16x16x128_f8f6f4 v[38:41], v[18:25], v[244:251], v[38:41], v208, v207 op_sel_hi:[0,0,0]
	s_setprio 0
	s_setprio 1
	v_mfma_scale_f32_16x16x128_f8f6f4 v[90:93], v[10:17], v[170:177], v[90:93], v208, v207 op_sel_hi:[0,0,0]
	v_mfma_scale_f32_16x16x128_f8f6f4 v[82:85], v[2:9], v[170:177], v[82:85], v208, v207 op_sel_hi:[0,0,0]
	v_mfma_scale_f32_16x16x128_f8f6f4 v[74:77], v[10:17], v[214:221], v[74:77], v208, v207 op_sel_hi:[0,0,0]
	v_mfma_scale_f32_16x16x128_f8f6f4 v[66:69], v[2:9], v[214:221], v[66:69], v208, v207 op_sel_hi:[0,0,0]
	v_mfma_scale_f32_16x16x128_f8f6f4 v[58:61], v[10:17], v[236:243], v[58:61], v208, v207 op_sel_hi:[0,0,0]
	v_mfma_scale_f32_16x16x128_f8f6f4 v[50:53], v[2:9], v[236:243], v[50:53], v208, v207 op_sel_hi:[0,0,0]
	v_mfma_scale_f32_16x16x128_f8f6f4 v[42:45], v[10:17], v[244:251], v[42:45], v208, v207 op_sel_hi:[0,0,0]
	v_mfma_scale_f32_16x16x128_f8f6f4 v[34:37], v[2:9], v[244:251], v[34:37], v208, v207 op_sel_hi:[0,0,0]
	s_setprio 0
	s_barrier
	s_cmp_lt_i32 s55, s11
	s_cbranch_scc0 .LBB0_1841
	s_mov_b64 s[64:65], s[60:61]
	s_branch .LBB0_1836
